# gu unit header: one drain instead of two; scan consumer waves run at s_setprio 2 inside the chunk loop
# speedup vs baseline: 1.0260x; 1.0042x over previous
.LBB0_418:
	s_setprio 2
	v_add_u32_e32 v106, v192, v193
	v_add_u32_e32 v101, v203, v202
	ds_read_b128 v[64:67], v106
	ds_read_b128 v[68:71], v106 offset:64
	ds_read_b128 v[72:75], v101 offset:34816
	ds_read_b128 v[76:79], v101 offset:34880
	ds_read_b128 v[80:83], v101 offset:39168
	ds_read_b128 v[84:87], v101 offset:39232
	ds_read_b128 v[88:91], v101 offset:43520
	ds_read_b128 v[92:95], v101 offset:43584
	ds_read_b128 v[102:105], v101 offset:47872
	ds_read_b128 v[108:111], v101 offset:47936
	ds_read_b128 v[112:115], v106 offset:128
	ds_read_b128 v[116:119], v106 offset:192
	ds_read_b128 v[120:123], v101 offset:34944
	ds_read_b128 v[124:127], v101 offset:35008
	ds_read_b128 v[128:131], v101 offset:39296
	ds_read_b128 v[132:135], v101 offset:39360
	ds_read_b128 v[136:139], v101 offset:43648
	ds_read_b128 v[140:143], v101 offset:43712
	ds_read_b128 v[144:147], v101 offset:48000
	ds_read_b128 v[148:151], v101 offset:48064
	s_waitcnt lgkmcnt(14)
	v_mfma_f32_16x16x32_bf16 v[72:75], v[72:75], v[64:67], 0
	v_add_u32_e32 v107, v195, v207
	v_mfma_f32_16x16x32_bf16 v[72:75], v[76:79], v[68:71], v[72:75]
	v_mfma_f32_16x16x32_bf16 v[80:83], v[80:83], v[64:67], 0
	s_waitcnt lgkmcnt(7)
	v_mfma_f32_16x16x32_bf16 v[72:75], v[120:123], v[112:115], v[72:75]
	v_mfma_f32_16x16x32_bf16 v[76:79], v[84:87], v[68:71], v[80:83]
	s_waitcnt lgkmcnt(6)
	v_mfma_f32_16x16x32_bf16 v[72:75], v[124:127], v[116:119], v[72:75]
	v_mfma_f32_16x16x32_bf16 v[88:91], v[88:91], v[64:67], 0
	v_mfma_f32_16x16x32_bf16 v[64:67], v[102:105], v[64:67], 0
	s_nop 5
	v_cndmask_b32_e32 v72, 0, v72, vcc
	v_cndmask_b32_e64 v73, 0, v73, s[52:53]
	v_cndmask_b32_e64 v74, 0, v74, s[54:55]
	s_waitcnt lgkmcnt(5)
	v_mfma_f32_16x16x32_bf16 v[76:79], v[128:131], v[112:115], v[76:79]
	v_cndmask_b32_e64 v75, 0, v75, s[56:57]
	v_cvt_pk_bf16_f32 v80, v72, v73
	v_cvt_pk_bf16_f32 v81, v74, v75
	s_waitcnt lgkmcnt(4)
	v_mfma_f32_16x16x32_bf16 v[72:75], v[132:135], v[116:119], v[76:79]
	v_add_u32_e32 v104, v195, v196
	ds_write_b64 v104, v[80:81]
	v_add_u32_e32 v105, v195, v205
	v_mfma_f32_16x16x32_bf16 v[76:79], v[92:95], v[68:71], v[88:91]
	v_mfma_f32_16x16x32_bf16 v[64:67], v[108:111], v[68:71], v[64:67]
	s_nop 2
	v_cndmask_b32_e64 v80, 0, v72, s[58:59]
	v_cndmask_b32_e64 v81, 0, v73, s[60:61]
	v_cndmask_b32_e64 v82, 0, v74, s[62:63]
	v_cndmask_b32_e64 v83, 0, v75, s[64:65]
	s_waitcnt lgkmcnt(4)
	v_mfma_f32_16x16x32_bf16 v[72:75], v[136:139], v[112:115], v[76:79]
	v_add_u32_e32 v108, v195, v209
	s_waitcnt lgkmcnt(2)
	v_mfma_f32_16x16x32_bf16 v[64:67], v[144:147], v[112:115], v[64:67]
	v_cvt_pk_bf16_f32 v76, v80, v81
	v_cvt_pk_bf16_f32 v77, v82, v83
	ds_write_b64 v105, v[76:77]
	v_mfma_f32_16x16x32_bf16 v[72:75], v[140:143], v[116:119], v[72:75]
	s_waitcnt lgkmcnt(2)
	v_mfma_f32_16x16x32_bf16 v[64:67], v[148:151], v[116:119], v[64:67]
	s_nop 5
	v_cndmask_b32_e64 v72, 0, v72, s[66:67]
	v_cndmask_b32_e64 v73, 0, v73, s[68:69]
	v_cndmask_b32_e64 v69, 0, v74, s[70:71]
	v_cndmask_b32_e64 v70, 0, v75, s[72:73]
	v_cndmask_b32_e64 v64, 0, v64, s[74:75]
	v_cndmask_b32_e64 v65, 0, v65, s[76:77]
	v_cndmask_b32_e64 v66, 0, v66, s[78:79]
	v_cndmask_b32_e64 v67, 0, v67, s[80:81]
	v_cvt_pk_bf16_f32 v68, v72, v73
	v_cvt_pk_bf16_f32 v69, v69, v70
	v_cvt_pk_bf16_f32 v64, v64, v65
	v_cvt_pk_bf16_f32 v65, v66, v67
	ds_write_b64 v107, v[68:69]
	ds_write_b64 v108, v[64:65]
	v_add_u32_e32 v103, v197, v202
	v_add_u32_e32 v97, 0x1000, v103
	v_add_u32_e32 v102, 0x2000, v103
	v_add_u32_e32 v109, 0x3000, v103
	ds_read2_b64 v[64:67], v103 offset1:4
	ds_read2_b64 v[68:71], v97 offset0:32 offset1:36
	ds_read2_b64 v[72:75], v102 offset0:64 offset1:68
	ds_read2_b64 v[76:79], v109 offset0:96 offset1:100
	ds_read2_b64 v[80:83], v103 offset0:8 offset1:12
	ds_read2_b64 v[84:87], v97 offset0:40 offset1:44
	ds_read2_b64 v[88:91], v102 offset0:72 offset1:76
	ds_read2_b64 v[92:95], v109 offset0:104 offset1:108
	ds_read2_b64 v[110:113], v103 offset0:16 offset1:20
	ds_read2_b64 v[114:117], v97 offset0:48 offset1:52
	ds_read2_b64 v[118:121], v102 offset0:80 offset1:84
	ds_read2_b64 v[122:125], v109 offset0:112 offset1:116
	ds_read2_b64 v[126:129], v103 offset0:24 offset1:28
	ds_read2_b64 v[130:133], v97 offset0:56 offset1:60
	ds_read2_b64 v[134:137], v102 offset0:88 offset1:92
	ds_read2_b64 v[138:141], v109 offset0:120 offset1:124
	v_cvt_pk_bf16_f32 v142, v0, v1
	v_cvt_pk_bf16_f32 v143, v2, v3
	v_cvt_pk_bf16_f32 v144, v8, v9
	v_cvt_pk_bf16_f32 v145, v10, v11
	v_cvt_pk_bf16_f32 v146, v4, v5
	v_cvt_pk_bf16_f32 v147, v6, v7
	v_cvt_pk_bf16_f32 v148, v12, v13
	v_cvt_pk_bf16_f32 v149, v14, v15
	s_waitcnt lgkmcnt(14)
	v_mfma_f32_16x16x32_bf16 v[150:153], v[142:145], v[64:67], 0
	v_cvt_pk_bf16_f32 v162, v16, v17
	v_cvt_pk_bf16_f32 v163, v18, v19
	v_cvt_pk_bf16_f32 v164, v24, v25
	v_mfma_f32_16x16x32_bf16 v[64:67], v[146:149], v[64:67], 0
	v_cvt_pk_bf16_f32 v165, v26, v27
	v_mfma_f32_16x16x32_bf16 v[154:157], v[142:145], v[68:71], 0
	v_mfma_f32_16x16x32_bf16 v[68:71], v[146:149], v[68:71], 0
	s_waitcnt lgkmcnt(13)
	v_mfma_f32_16x16x32_bf16 v[158:161], v[142:145], v[72:75], 0
	v_mfma_f32_16x16x32_bf16 v[72:75], v[146:149], v[72:75], 0
	s_waitcnt lgkmcnt(12)
	v_mfma_f32_16x16x32_bf16 v[142:145], v[142:145], v[76:79], 0
	v_mfma_f32_16x16x32_bf16 v[76:79], v[146:149], v[76:79], 0
	v_cvt_pk_bf16_f32 v146, v20, v21
	v_cvt_pk_bf16_f32 v147, v22, v23
	v_cvt_pk_bf16_f32 v148, v28, v29
	v_cvt_pk_bf16_f32 v149, v30, v31
	s_waitcnt lgkmcnt(11)
	v_mfma_f32_16x16x32_bf16 v[150:153], v[162:165], v[80:83], v[150:153]
	v_mfma_f32_16x16x32_bf16 v[64:67], v[146:149], v[80:83], v[64:67]
	s_waitcnt lgkmcnt(10)
	v_mfma_f32_16x16x32_bf16 v[80:83], v[162:165], v[84:87], v[154:157]
	v_mfma_f32_16x16x32_bf16 v[68:71], v[146:149], v[84:87], v[68:71]
	s_waitcnt lgkmcnt(9)
	v_mfma_f32_16x16x32_bf16 v[84:87], v[162:165], v[88:91], v[158:161]
	v_mfma_f32_16x16x32_bf16 v[72:75], v[146:149], v[88:91], v[72:75]
	s_waitcnt lgkmcnt(8)
	v_mfma_f32_16x16x32_bf16 v[88:91], v[162:165], v[92:95], v[142:145]
	s_nop 2
	v_cvt_pk_bf16_f32 v142, v32, v33
	v_cvt_pk_bf16_f32 v143, v34, v35
	v_cvt_pk_bf16_f32 v144, v40, v41
	v_cvt_pk_bf16_f32 v145, v42, v43
	v_mfma_f32_16x16x32_bf16 v[76:79], v[146:149], v[92:95], v[76:79]
	v_cvt_pk_bf16_f32 v92, v36, v37
	v_cvt_pk_bf16_f32 v93, v38, v39
	v_cvt_pk_bf16_f32 v94, v44, v45
	v_cvt_pk_bf16_f32 v95, v46, v47
	s_waitcnt lgkmcnt(7)
	v_mfma_f32_16x16x32_bf16 v[146:149], v[142:145], v[110:113], v[150:153]
	v_mfma_f32_16x16x32_bf16 v[64:67], v[92:95], v[110:113], v[64:67]
	v_cvt_pk_bf16_f32 v110, v48, v49
	v_cvt_pk_bf16_f32 v111, v50, v51
	v_cvt_pk_bf16_f32 v112, v56, v57
	s_waitcnt lgkmcnt(6)
	v_mfma_f32_16x16x32_bf16 v[68:71], v[92:95], v[114:117], v[68:71]
	v_cvt_pk_bf16_f32 v113, v58, v59
	s_waitcnt lgkmcnt(5)
	v_mfma_f32_16x16x32_bf16 v[72:75], v[92:95], v[118:121], v[72:75]
	s_waitcnt lgkmcnt(4)
	v_mfma_f32_16x16x32_bf16 v[76:79], v[92:95], v[122:125], v[76:79]
	v_cvt_pk_bf16_f32 v92, v52, v53
	v_cvt_pk_bf16_f32 v93, v54, v55
	v_cvt_pk_bf16_f32 v94, v60, v61
	v_cvt_pk_bf16_f32 v95, v62, v63
	v_mfma_f32_16x16x32_bf16 v[80:83], v[142:145], v[114:117], v[80:83]
	v_mfma_f32_16x16x32_bf16 v[84:87], v[142:145], v[118:121], v[84:87]
	v_mfma_f32_16x16x32_bf16 v[88:91], v[142:145], v[122:125], v[88:91]
	s_waitcnt lgkmcnt(3)
	v_mfma_f32_16x16x32_bf16 v[114:117], v[110:113], v[126:129], v[146:149]
	v_mfma_f32_16x16x32_bf16 v[64:67], v[92:95], v[126:129], v[64:67]
	s_waitcnt lgkmcnt(2)
	v_mfma_f32_16x16x32_bf16 v[80:83], v[110:113], v[130:133], v[80:83]
	v_mfma_f32_16x16x32_bf16 v[68:71], v[92:95], v[130:133], v[68:71]
	s_waitcnt lgkmcnt(1)
	v_mfma_f32_16x16x32_bf16 v[84:87], v[110:113], v[134:137], v[84:87]
	v_mfma_f32_16x16x32_bf16 v[72:75], v[92:95], v[134:137], v[72:75]
	s_waitcnt lgkmcnt(0)
	v_mfma_f32_16x16x32_bf16 v[88:91], v[110:113], v[138:141], v[88:91]
	v_mfma_f32_16x16x32_bf16 v[76:79], v[92:95], v[138:141], v[76:79]
	v_add_u32_e32 v97, v198, v210
	ds_read_b64_tr_b16 v[94:95], v97 offset:1088
	ds_read_b64_tr_b16 v[92:93], v97
	ds_read_b64_tr_b16 v[112:113], v97 offset:1120
	ds_read_b64_tr_b16 v[110:111], v97 offset:32
	ds_read_b64_tr_b16 v[118:119], v97 offset:8704
	ds_read_b64_tr_b16 v[120:121], v97 offset:9792
	ds_read_b64_tr_b16 v[124:125], v97 offset:9824
	ds_read_b64_tr_b16 v[122:123], v97 offset:8736
	ds_read_b64_tr_b16 v[126:127], v211 offset:34816
	ds_read_b64_tr_b16 v[130:131], v211 offset:34848
	ds_read_b64_tr_b16 v[134:135], v211 offset:34880
	ds_read_b64_tr_b16 v[138:139], v211 offset:34912
	ds_read_b64_tr_b16 v[128:129], v211 offset:35904
	ds_read_b64_tr_b16 v[132:133], v211 offset:35936
	ds_read_b64_tr_b16 v[136:137], v211 offset:35968
	ds_read_b64_tr_b16 v[140:141], v211 offset:36000
	ds_read_b64_tr_b16 v[142:143], v211 offset:34944
	ds_read_b64_tr_b16 v[146:147], v211 offset:34976
	ds_read_b64_tr_b16 v[150:151], v211 offset:35008
	ds_read_b64_tr_b16 v[154:155], v211 offset:35040
	ds_read_b64_tr_b16 v[144:145], v211 offset:36032
	ds_read_b64_tr_b16 v[148:149], v211 offset:36064
	ds_read_b64_tr_b16 v[152:153], v211 offset:36096
	ds_read_b64_tr_b16 v[156:157], v211 offset:36128
	ds_read_b64_tr_b16 v[158:159], v211 offset:43520
	ds_read_b64_tr_b16 v[162:163], v211 offset:43552
	ds_read_b64_tr_b16 v[166:167], v211 offset:43584
	ds_read_b64_tr_b16 v[182:183], v211 offset:43616
	ds_read_b64_tr_b16 v[160:161], v211 offset:44608
	ds_read_b64_tr_b16 v[164:165], v211 offset:44640
	ds_read_b64_tr_b16 v[168:169], v211 offset:44672
	ds_read_b64_tr_b16 v[184:185], v211 offset:44704
	ds_read_b64_tr_b16 v[186:187], v211 offset:43648
	ds_read_b64_tr_b16 v[232:233], v211 offset:43680
	ds_read_b64_tr_b16 v[236:237], v211 offset:43712
	ds_read_b64_tr_b16 v[240:241], v211 offset:43744
	ds_read_b64_tr_b16 v[188:189], v211 offset:44736
	ds_read_b64_tr_b16 v[234:235], v211 offset:44768
	ds_read_b64_tr_b16 v[238:239], v211 offset:44800
	ds_read_b64_tr_b16 v[242:243], v211 offset:44832
	s_waitcnt lgkmcnt(14)
	v_mfma_f32_16x16x32_bf16 v[0:3], v[126:129], v[92:95], v[0:3]
	v_add_u32_e32 v102, v199, v212
	s_waitcnt lgkmcnt(0)
	s_barrier
	v_mfma_f32_16x16x32_bf16 v[4:7], v[126:129], v[110:113], v[4:7]
	v_mfma_f32_16x16x32_bf16 v[8:11], v[130:133], v[92:95], v[8:11]
	v_mfma_f32_16x16x32_bf16 v[12:15], v[130:133], v[110:113], v[12:15]
	v_mfma_f32_16x16x32_bf16 v[16:19], v[134:137], v[92:95], v[16:19]
	v_mfma_f32_16x16x32_bf16 v[20:23], v[134:137], v[110:113], v[20:23]
	v_mfma_f32_16x16x32_bf16 v[24:27], v[138:141], v[92:95], v[24:27]
	v_mfma_f32_16x16x32_bf16 v[28:31], v[138:141], v[110:113], v[28:31]
	ds_read_b128 v[126:129], v102
	ds_read_b128 v[130:133], v102 offset:64
	ds_read_b128 v[134:137], v102 offset:2304
	ds_read_b128 v[138:141], v102 offset:2368
	v_mfma_f32_16x16x32_bf16 v[32:35], v[142:145], v[92:95], v[32:35]
	v_mfma_f32_16x16x32_bf16 v[36:39], v[142:145], v[110:113], v[36:39]
	v_mfma_f32_16x16x32_bf16 v[40:43], v[146:149], v[92:95], v[40:43]
	v_mfma_f32_16x16x32_bf16 v[44:47], v[146:149], v[110:113], v[44:47]
	v_mfma_f32_16x16x32_bf16 v[48:51], v[150:153], v[92:95], v[48:51]
	v_mfma_f32_16x16x32_bf16 v[52:55], v[150:153], v[110:113], v[52:55]
	v_mfma_f32_16x16x32_bf16 v[56:59], v[154:157], v[92:95], v[56:59]
	v_mfma_f32_16x16x32_bf16 v[60:63], v[154:157], v[110:113], v[60:63]
	ds_read_b128 v[142:145], v102 offset:4608
	ds_read_b128 v[146:149], v102 offset:4672
	ds_read_b128 v[150:153], v102 offset:6912
	ds_read_b128 v[154:157], v102 offset:6976
	v_mfma_f32_16x16x32_bf16 v[0:3], v[158:161], v[118:121], v[0:3]
	v_mfma_f32_16x16x32_bf16 v[4:7], v[158:161], v[122:125], v[4:7]
	v_mfma_f32_16x16x32_bf16 v[8:11], v[162:165], v[118:121], v[8:11]
	v_mfma_f32_16x16x32_bf16 v[12:15], v[162:165], v[122:125], v[12:15]
	v_mfma_f32_16x16x32_bf16 v[16:19], v[166:169], v[118:121], v[16:19]
	v_mfma_f32_16x16x32_bf16 v[20:23], v[166:169], v[122:125], v[20:23]
	v_mfma_f32_16x16x32_bf16 v[24:27], v[182:185], v[118:121], v[24:27]
	v_mfma_f32_16x16x32_bf16 v[28:31], v[182:185], v[122:125], v[28:31]
	v_mfma_f32_16x16x32_bf16 v[32:35], v[186:189], v[118:121], v[32:35]
	v_mfma_f32_16x16x32_bf16 v[36:39], v[186:189], v[122:125], v[36:39]
	v_mfma_f32_16x16x32_bf16 v[40:43], v[232:235], v[118:121], v[40:43]
	v_mfma_f32_16x16x32_bf16 v[44:47], v[232:235], v[122:125], v[44:47]
	v_mfma_f32_16x16x32_bf16 v[48:51], v[236:239], v[118:121], v[48:51]
	v_mfma_f32_16x16x32_bf16 v[52:55], v[236:239], v[122:125], v[52:55]
	v_mfma_f32_16x16x32_bf16 v[56:59], v[240:243], v[118:121], v[56:59]
	v_mfma_f32_16x16x32_bf16 v[60:63], v[240:243], v[122:125], v[60:63]
	s_waitcnt lgkmcnt(7)
	v_mfma_f32_16x16x32_bf16 v[114:117], v[92:95], v[126:129], v[114:117]
	v_mov_b32_e32 v97, v96
	v_pk_mul_f32 v[2:3], v[96:97], v[2:3]
	v_pk_mul_f32 v[0:1], v[98:99], v[0:1]
	v_mfma_f32_16x16x32_bf16 v[64:67], v[110:113], v[126:129], v[64:67]
	v_mul_f32_e64 v6, v96, v6
	v_mul_f32_e64 v7, v97, v7
	v_pk_mul_f32 v[4:5], v[98:99], v[4:5]
	v_pk_mul_f32 v[10:11], v[96:97], v[10:11]
	s_waitcnt lgkmcnt(5)
	v_mfma_f32_16x16x32_bf16 v[80:83], v[92:95], v[134:137], v[80:83]
	v_mul_f32_e64 v8, v98, v8
	v_mul_f32_e64 v9, v99, v9
	v_pk_mul_f32 v[14:15], v[96:97], v[14:15]
	v_pk_mul_f32 v[12:13], v[98:99], v[12:13]
	v_mfma_f32_16x16x32_bf16 v[68:71], v[110:113], v[134:137], v[68:71]
	v_mul_f32_e64 v18, v96, v18
	v_mul_f32_e64 v19, v97, v19
	v_pk_mul_f32 v[16:17], v[98:99], v[16:17]
	v_pk_mul_f32 v[22:23], v[96:97], v[22:23]
	s_waitcnt lgkmcnt(3)
	v_mfma_f32_16x16x32_bf16 v[126:129], v[92:95], v[142:145], v[84:87]
	v_mul_f32_e64 v20, v98, v20
	v_mul_f32_e64 v21, v99, v21
	v_pk_mul_f32 v[26:27], v[96:97], v[26:27]
	v_pk_mul_f32 v[24:25], v[98:99], v[24:25]
	v_mfma_f32_16x16x32_bf16 v[72:75], v[110:113], v[142:145], v[72:75]
	v_mul_f32_e64 v30, v96, v30
	v_mul_f32_e64 v31, v97, v31
	v_pk_mul_f32 v[28:29], v[98:99], v[28:29]
	v_pk_mul_f32 v[34:35], v[96:97], v[34:35]
	s_waitcnt lgkmcnt(1)
	v_mfma_f32_16x16x32_bf16 v[134:137], v[92:95], v[150:153], v[88:91]
	v_mul_f32_e64 v32, v98, v32
	v_mul_f32_e64 v33, v99, v33
	v_pk_mul_f32 v[38:39], v[96:97], v[38:39]
	v_pk_mul_f32 v[36:37], v[98:99], v[36:37]
	v_mfma_f32_16x16x32_bf16 v[110:113], v[110:113], v[150:153], v[76:79]
	v_mul_f32_e64 v42, v96, v42
	v_mul_f32_e64 v43, v97, v43
	v_pk_mul_f32 v[40:41], v[98:99], v[40:41]
	v_pk_mul_f32 v[46:47], v[96:97], v[46:47]
	v_mfma_f32_16x16x32_bf16 v[92:95], v[118:121], v[130:133], v[114:117]
	v_mul_f32_e64 v44, v98, v44
	v_mul_f32_e64 v45, v99, v45
	v_pk_mul_f32 v[50:51], v[96:97], v[50:51]
	v_pk_mul_f32 v[48:49], v[98:99], v[48:49]
	v_mfma_f32_16x16x32_bf16 v[88:91], v[122:125], v[130:133], v[64:67]
	v_mul_f32_e64 v54, v96, v54
	v_mul_f32_e64 v55, v97, v55
	v_pk_mul_f32 v[52:53], v[98:99], v[52:53]
	v_pk_mul_f32 v[58:59], v[96:97], v[58:59]
	v_mfma_f32_16x16x32_bf16 v[84:87], v[118:121], v[138:141], v[80:83]
	v_mul_f32_e64 v56, v98, v56
	v_mul_f32_e64 v57, v99, v57
	s_nop 0
	v_cvt_pk_bf16_f32 v88, v88, v89
	v_cvt_pk_bf16_f32 v89, v90, v91
	v_mfma_f32_16x16x32_bf16 v[80:83], v[122:125], v[138:141], v[68:71]
	v_mul_f32_e64 v62, v96, v62
	v_mul_f32_e64 v63, v97, v63
	v_cvt_pk_bf16_f32 v84, v84, v85
	v_cvt_pk_bf16_f32 v85, v86, v87
	v_mfma_f32_16x16x32_bf16 v[76:79], v[118:121], v[146:149], v[126:129]
	v_mul_f32_e64 v60, v98, v60
	v_mul_f32_e64 v61, v99, v61
	s_nop 0
	v_cvt_pk_bf16_f32 v86, v80, v81
	v_cvt_pk_bf16_f32 v87, v82, v83
	v_mfma_f32_16x16x32_bf16 v[72:75], v[122:125], v[146:149], v[72:75]
	s_waitcnt lgkmcnt(0)
	v_mfma_f32_16x16x32_bf16 v[68:71], v[118:121], v[154:157], v[134:137]
	v_cvt_pk_bf16_f32 v76, v76, v77
	v_cvt_pk_bf16_f32 v77, v78, v79
	s_nop 3
	v_cvt_pk_bf16_f32 v78, v72, v73
	v_mfma_f32_16x16x32_bf16 v[64:67], v[122:125], v[154:157], v[110:113]
	v_cvt_pk_bf16_f32 v79, v74, v75
	v_cvt_pk_bf16_f32 v68, v68, v69
	v_cvt_pk_bf16_f32 v69, v70, v71
	v_cvt_pk_bf16_f32 v110, v92, v93
	v_add_u32_e32 v92, v200, v202
	v_cvt_pk_bf16_f32 v111, v94, v95
	v_add_u32_e32 v80, 0x1000, v92
	v_add_u32_e32 v72, 0x2000, v92
	v_cvt_pk_bf16_f32 v70, v64, v65
	v_cvt_pk_bf16_f32 v71, v66, v67
	v_add_u32_e32 v64, 0x3000, v92
	ds_write2_b64 v92, v[110:111], v[88:89] offset1:4
	ds_write2_b64 v80, v[84:85], v[86:87] offset0:32 offset1:36
	ds_write2_b64 v72, v[76:77], v[78:79] offset0:64 offset1:68
	ds_write2_b64 v64, v[68:69], v[70:71] offset0:96 offset1:100
	s_waitcnt lgkmcnt(0)
	s_barrier
	ds_read_b128 v[66:69], v106 offset:17408
	ds_read_b128 v[74:77], v101 offset:52224
	ds_read_b128 v[82:85], v101 offset:56576
	ds_read_b128 v[86:89], v101 offset:60928
	ds_read_b128 v[110:113], v101 offset:65280
	ds_read_b128 v[114:117], v106 offset:17472
	ds_read_b128 v[118:121], v101 offset:52288
	ds_read_b128 v[122:125], v101 offset:56640
	ds_read_b128 v[126:129], v101 offset:60992
	ds_read_b128 v[130:133], v101 offset:65344
	ds_read_b128 v[134:137], v106 offset:17536
	ds_read_b128 v[138:141], v101 offset:52352
	ds_read_b128 v[142:145], v101 offset:56704
	ds_read_b128 v[146:149], v101 offset:61056
	ds_read_b128 v[150:153], v101 offset:65408
	ds_read_b128 v[154:157], v106 offset:17600
	ds_read_b128 v[158:161], v101 offset:52416
	ds_read_b128 v[162:165], v101 offset:56768
	ds_read_b128 v[166:169], v101 offset:61120
	ds_read_b128 v[182:185], v101 offset:65472
	s_waitcnt lgkmcnt(14)
	v_mfma_f32_16x16x32_bf16 v[74:77], v[74:77], v[66:69], 0
	v_mfma_f32_16x16x32_bf16 v[82:85], v[82:85], v[66:69], 0
	s_waitcnt lgkmcnt(13)
	v_mfma_f32_16x16x32_bf16 v[74:77], v[118:121], v[114:117], v[74:77]
	v_mfma_f32_16x16x32_bf16 v[86:89], v[86:89], v[66:69], 0
	s_waitcnt lgkmcnt(12)
	v_mfma_f32_16x16x32_bf16 v[82:85], v[122:125], v[114:117], v[82:85]
	s_waitcnt lgkmcnt(8)
	v_mfma_f32_16x16x32_bf16 v[74:77], v[138:141], v[134:137], v[74:77]
	v_mfma_f32_16x16x32_bf16 v[66:69], v[110:113], v[66:69], 0
	v_mfma_f32_16x16x32_bf16 v[86:89], v[126:129], v[114:117], v[86:89]
	s_waitcnt lgkmcnt(3)
	v_mfma_f32_16x16x32_bf16 v[74:77], v[158:161], v[154:157], v[74:77]
	v_mfma_f32_16x16x32_bf16 v[82:85], v[142:145], v[134:137], v[82:85]
	v_mfma_f32_16x16x32_bf16 v[66:69], v[130:133], v[114:117], v[66:69]
	s_nop 5
	v_cndmask_b32_e32 v65, 0, v74, vcc
	v_cndmask_b32_e64 v70, 0, v75, s[52:53]
	v_cndmask_b32_e64 v71, 0, v76, s[54:55]
	v_cndmask_b32_e64 v73, 0, v77, s[56:57]
	s_waitcnt lgkmcnt(2)
	v_mfma_f32_16x16x32_bf16 v[74:77], v[162:165], v[154:157], v[82:85]
	v_cvt_pk_bf16_f32 v70, v65, v70
	v_cvt_pk_bf16_f32 v71, v71, v73
	ds_write_b64 v104, v[70:71]
	v_mfma_f32_16x16x32_bf16 v[82:85], v[146:149], v[134:137], v[86:89]
	v_mfma_f32_16x16x32_bf16 v[66:69], v[150:153], v[134:137], v[66:69]
	s_nop 2
	v_cndmask_b32_e64 v65, 0, v74, s[58:59]
	v_cndmask_b32_e64 v70, 0, v75, s[60:61]
	v_cndmask_b32_e64 v71, 0, v76, s[62:63]
	v_cndmask_b32_e64 v73, 0, v77, s[64:65]
	s_waitcnt lgkmcnt(2)
	v_mfma_f32_16x16x32_bf16 v[74:77], v[166:169], v[154:157], v[82:85]
	v_cvt_pk_bf16_f32 v70, v65, v70
	v_cvt_pk_bf16_f32 v71, v71, v73
	ds_write_b64 v105, v[70:71]
	s_waitcnt lgkmcnt(2)
	v_mfma_f32_16x16x32_bf16 v[66:69], v[182:185], v[154:157], v[66:69]
	s_nop 2
	v_cndmask_b32_e64 v65, 0, v74, s[66:67]
	v_cndmask_b32_e64 v70, 0, v75, s[68:69]
	v_cndmask_b32_e64 v71, 0, v76, s[70:71]
	v_cndmask_b32_e64 v73, 0, v77, s[72:73]
	v_cvt_pk_bf16_f32 v70, v65, v70
	v_cndmask_b32_e64 v65, 0, v66, s[74:75]
	v_cndmask_b32_e64 v66, 0, v67, s[76:77]
	v_cndmask_b32_e64 v67, 0, v68, s[78:79]
	v_cndmask_b32_e64 v68, 0, v69, s[80:81]
	v_cvt_pk_bf16_f32 v71, v71, v73
	v_cvt_pk_bf16_f32 v66, v65, v66
	v_cvt_pk_bf16_f32 v67, v67, v68
	ds_write_b64 v107, v[70:71]
	ds_write_b64 v108, v[66:67]
	v_add_u32_e32 v65, 0x4000, v103
	v_add_u32_e32 v70, 0x5000, v103
	v_add_u32_e32 v71, 0x6000, v103
	v_add_u32_e32 v73, 0x7000, v103
	ds_read2_b64 v[66:69], v65 offset0:128 offset1:132
	ds_read2_b64 v[74:77], v70 offset0:160 offset1:164
	ds_read2_b64 v[82:85], v71 offset0:192 offset1:196
	ds_read2_b64 v[86:89], v73 offset0:224 offset1:228
	ds_read2_b64 v[104:107], v65 offset0:136 offset1:140
	ds_read2_b64 v[108:111], v70 offset0:168 offset1:172
	ds_read2_b64 v[112:115], v71 offset0:200 offset1:204
	ds_read2_b64 v[116:119], v73 offset0:232 offset1:236
	ds_read2_b64 v[120:123], v65 offset0:144 offset1:148
	ds_read2_b64 v[124:127], v70 offset0:176 offset1:180
	ds_read2_b64 v[128:131], v71 offset0:208 offset1:212
	ds_read2_b64 v[132:135], v73 offset0:240 offset1:244
	ds_read2_b64 v[136:139], v65 offset0:152 offset1:156
	ds_read2_b64 v[140:143], v70 offset0:184 offset1:188
	ds_read2_b64 v[144:147], v71 offset0:216 offset1:220
	ds_read2_b64 v[148:151], v73 offset0:248 offset1:252
	v_cvt_pk_bf16_f32 v152, v0, v1
	v_cvt_pk_bf16_f32 v153, v2, v3
	v_cvt_pk_bf16_f32 v154, v8, v9
	v_cvt_pk_bf16_f32 v155, v10, v11
	v_cvt_pk_bf16_f32 v156, v4, v5
	v_cvt_pk_bf16_f32 v157, v6, v7
	v_cvt_pk_bf16_f32 v158, v12, v13
	v_cvt_pk_bf16_f32 v159, v14, v15
	s_waitcnt lgkmcnt(14)
	v_mfma_f32_16x16x32_bf16 v[160:163], v[152:155], v[66:69], 0
	v_cvt_pk_bf16_f32 v182, v16, v17
	v_cvt_pk_bf16_f32 v183, v18, v19
	v_cvt_pk_bf16_f32 v184, v24, v25
	v_mfma_f32_16x16x32_bf16 v[66:69], v[156:159], v[66:69], 0
	v_cvt_pk_bf16_f32 v185, v26, v27
	v_mfma_f32_16x16x32_bf16 v[164:167], v[152:155], v[74:77], 0
	v_mfma_f32_16x16x32_bf16 v[74:77], v[156:159], v[74:77], 0
	s_waitcnt lgkmcnt(13)
	v_mfma_f32_16x16x32_bf16 v[168:171], v[152:155], v[82:85], 0
	v_mfma_f32_16x16x32_bf16 v[82:85], v[156:159], v[82:85], 0
	s_waitcnt lgkmcnt(12)
	v_mfma_f32_16x16x32_bf16 v[152:155], v[152:155], v[86:89], 0
	v_mfma_f32_16x16x32_bf16 v[86:89], v[156:159], v[86:89], 0
	v_cvt_pk_bf16_f32 v156, v20, v21
	v_cvt_pk_bf16_f32 v157, v22, v23
	v_cvt_pk_bf16_f32 v158, v28, v29
	v_cvt_pk_bf16_f32 v159, v30, v31
	s_waitcnt lgkmcnt(11)
	v_mfma_f32_16x16x32_bf16 v[160:163], v[182:185], v[104:107], v[160:163]
	v_mfma_f32_16x16x32_bf16 v[66:69], v[156:159], v[104:107], v[66:69]
	s_waitcnt lgkmcnt(10)
	v_mfma_f32_16x16x32_bf16 v[104:107], v[182:185], v[108:111], v[164:167]
	v_mfma_f32_16x16x32_bf16 v[74:77], v[156:159], v[108:111], v[74:77]
	s_waitcnt lgkmcnt(9)
	v_mfma_f32_16x16x32_bf16 v[108:111], v[182:185], v[112:115], v[168:171]
	v_mfma_f32_16x16x32_bf16 v[82:85], v[156:159], v[112:115], v[82:85]
	s_waitcnt lgkmcnt(8)
	v_mfma_f32_16x16x32_bf16 v[112:115], v[182:185], v[116:119], v[152:155]
	s_nop 2
	v_cvt_pk_bf16_f32 v152, v32, v33
	v_cvt_pk_bf16_f32 v153, v34, v35
	v_cvt_pk_bf16_f32 v154, v40, v41
	v_cvt_pk_bf16_f32 v155, v42, v43
	v_mfma_f32_16x16x32_bf16 v[86:89], v[156:159], v[116:119], v[86:89]
	v_cvt_pk_bf16_f32 v116, v36, v37
	v_cvt_pk_bf16_f32 v117, v38, v39
	v_cvt_pk_bf16_f32 v118, v44, v45
	v_cvt_pk_bf16_f32 v119, v46, v47
	s_waitcnt lgkmcnt(7)
	v_mfma_f32_16x16x32_bf16 v[156:159], v[152:155], v[120:123], v[160:163]
	v_mfma_f32_16x16x32_bf16 v[66:69], v[116:119], v[120:123], v[66:69]
	v_cvt_pk_bf16_f32 v120, v48, v49
	v_cvt_pk_bf16_f32 v121, v50, v51
	v_cvt_pk_bf16_f32 v122, v56, v57
	s_waitcnt lgkmcnt(6)
	v_mfma_f32_16x16x32_bf16 v[74:77], v[116:119], v[124:127], v[74:77]
	v_cvt_pk_bf16_f32 v123, v58, v59
	s_waitcnt lgkmcnt(5)
	v_mfma_f32_16x16x32_bf16 v[82:85], v[116:119], v[128:131], v[82:85]
	s_waitcnt lgkmcnt(4)
	v_mfma_f32_16x16x32_bf16 v[86:89], v[116:119], v[132:135], v[86:89]
	v_cvt_pk_bf16_f32 v116, v52, v53
	v_cvt_pk_bf16_f32 v117, v54, v55
	v_cvt_pk_bf16_f32 v118, v60, v61
	v_cvt_pk_bf16_f32 v119, v62, v63
	v_mfma_f32_16x16x32_bf16 v[104:107], v[152:155], v[124:127], v[104:107]
	v_mfma_f32_16x16x32_bf16 v[108:111], v[152:155], v[128:131], v[108:111]
	v_mfma_f32_16x16x32_bf16 v[112:115], v[152:155], v[132:135], v[112:115]
	s_waitcnt lgkmcnt(3)
	v_mfma_f32_16x16x32_bf16 v[124:127], v[120:123], v[136:139], v[156:159]
	v_mfma_f32_16x16x32_bf16 v[66:69], v[116:119], v[136:139], v[66:69]
	s_waitcnt lgkmcnt(2)
	v_mfma_f32_16x16x32_bf16 v[104:107], v[120:123], v[140:143], v[104:107]
	v_mfma_f32_16x16x32_bf16 v[74:77], v[116:119], v[140:143], v[74:77]
	s_waitcnt lgkmcnt(1)
	v_mfma_f32_16x16x32_bf16 v[108:111], v[120:123], v[144:147], v[108:111]
	v_mfma_f32_16x16x32_bf16 v[82:85], v[116:119], v[144:147], v[82:85]
	s_waitcnt lgkmcnt(0)
	v_mfma_f32_16x16x32_bf16 v[112:115], v[120:123], v[148:151], v[112:115]
	v_mfma_f32_16x16x32_bf16 v[86:89], v[116:119], v[148:151], v[86:89]
	v_add_u32_e32 v65, v201, v210
	ds_read_b64_tr_b16 v[118:119], v65 offset:1088
	ds_read_b64_tr_b16 v[116:117], v65
	ds_read_b64_tr_b16 v[122:123], v65 offset:1120
	ds_read_b64_tr_b16 v[120:121], v65 offset:32
	ds_read_b64_tr_b16 v[128:129], v65 offset:8704
	ds_read_b64_tr_b16 v[130:131], v65 offset:9792
	ds_read_b64_tr_b16 v[134:135], v65 offset:9824
	ds_read_b64_tr_b16 v[132:133], v65 offset:8736
	ds_read_b64_tr_b16 v[136:137], v211 offset:52224
	ds_read_b64_tr_b16 v[140:141], v211 offset:52256
	ds_read_b64_tr_b16 v[144:145], v211 offset:52288
	ds_read_b64_tr_b16 v[148:149], v211 offset:52320
	ds_read_b64_tr_b16 v[138:139], v211 offset:53312
	ds_read_b64_tr_b16 v[142:143], v211 offset:53344
	ds_read_b64_tr_b16 v[146:147], v211 offset:53376
	ds_read_b64_tr_b16 v[150:151], v211 offset:53408
	ds_read_b64_tr_b16 v[152:153], v211 offset:52352
	ds_read_b64_tr_b16 v[156:157], v211 offset:52384
	ds_read_b64_tr_b16 v[160:161], v211 offset:52416
	ds_read_b64_tr_b16 v[164:165], v211 offset:52448
	ds_read_b64_tr_b16 v[154:155], v211 offset:53440
	ds_read_b64_tr_b16 v[158:159], v211 offset:53472
	ds_read_b64_tr_b16 v[162:163], v211 offset:53504
	ds_read_b64_tr_b16 v[166:167], v211 offset:53536
	ds_read_b64_tr_b16 v[168:169], v211 offset:60928
	ds_read_b64_tr_b16 v[182:183], v211 offset:60960
	ds_read_b64_tr_b16 v[186:187], v211 offset:60992
	ds_read_b64_tr_b16 v[232:233], v211 offset:61024
	ds_read_b64_tr_b16 v[170:171], v211 offset:62016
	ds_read_b64_tr_b16 v[184:185], v211 offset:62048
	ds_read_b64_tr_b16 v[188:189], v211 offset:62080
	ds_read_b64_tr_b16 v[234:235], v211 offset:62112
	ds_read_b64_tr_b16 v[236:237], v211 offset:61056
	ds_read_b64_tr_b16 v[240:241], v211 offset:61088
	ds_read_b64_tr_b16 v[244:245], v211 offset:61120
	ds_read_b64_tr_b16 v[248:249], v211 offset:61152
	ds_read_b64_tr_b16 v[238:239], v211 offset:62144
	ds_read_b64_tr_b16 v[242:243], v211 offset:62176
	ds_read_b64_tr_b16 v[246:247], v211 offset:62208
	ds_read_b64_tr_b16 v[250:251], v211 offset:62240
	s_waitcnt lgkmcnt(14)
	v_mfma_f32_16x16x32_bf16 v[0:3], v[136:139], v[116:119], v[0:3]
	s_waitcnt lgkmcnt(0)
	s_barrier
	v_mfma_f32_16x16x32_bf16 v[4:7], v[136:139], v[120:123], v[4:7]
	v_mfma_f32_16x16x32_bf16 v[8:11], v[140:143], v[116:119], v[8:11]
	v_mfma_f32_16x16x32_bf16 v[12:15], v[140:143], v[120:123], v[12:15]
	v_mfma_f32_16x16x32_bf16 v[16:19], v[144:147], v[116:119], v[16:19]
	v_mfma_f32_16x16x32_bf16 v[20:23], v[144:147], v[120:123], v[20:23]
	v_mfma_f32_16x16x32_bf16 v[24:27], v[148:151], v[116:119], v[24:27]
	v_mfma_f32_16x16x32_bf16 v[28:31], v[148:151], v[120:123], v[28:31]
	ds_read_b128 v[136:139], v102
	ds_read_b128 v[140:143], v102 offset:64
	ds_read_b128 v[144:147], v102 offset:2304
	ds_read_b128 v[148:151], v102 offset:2368
	v_mfma_f32_16x16x32_bf16 v[32:35], v[152:155], v[116:119], v[32:35]
	v_mfma_f32_16x16x32_bf16 v[36:39], v[152:155], v[120:123], v[36:39]
	v_mfma_f32_16x16x32_bf16 v[40:43], v[156:159], v[116:119], v[40:43]
	v_mfma_f32_16x16x32_bf16 v[44:47], v[156:159], v[120:123], v[44:47]
	v_mfma_f32_16x16x32_bf16 v[48:51], v[160:163], v[116:119], v[48:51]
	v_mfma_f32_16x16x32_bf16 v[52:55], v[160:163], v[120:123], v[52:55]
	v_mfma_f32_16x16x32_bf16 v[56:59], v[164:167], v[116:119], v[56:59]
	v_mfma_f32_16x16x32_bf16 v[60:63], v[164:167], v[120:123], v[60:63]
	ds_read_b128 v[152:155], v102 offset:4608
	ds_read_b128 v[156:159], v102 offset:4672
	ds_read_b128 v[160:163], v102 offset:6912
	ds_read_b128 v[164:167], v102 offset:6976
	v_mfma_f32_16x16x32_bf16 v[0:3], v[168:171], v[128:131], v[0:3]
	v_mfma_f32_16x16x32_bf16 v[4:7], v[168:171], v[132:135], v[4:7]
	v_mfma_f32_16x16x32_bf16 v[8:11], v[182:185], v[128:131], v[8:11]
	v_mfma_f32_16x16x32_bf16 v[12:15], v[182:185], v[132:135], v[12:15]
	v_mfma_f32_16x16x32_bf16 v[16:19], v[186:189], v[128:131], v[16:19]
	v_mfma_f32_16x16x32_bf16 v[20:23], v[186:189], v[132:135], v[20:23]
	v_mfma_f32_16x16x32_bf16 v[24:27], v[232:235], v[128:131], v[24:27]
	v_mfma_f32_16x16x32_bf16 v[28:31], v[232:235], v[132:135], v[28:31]
	v_mfma_f32_16x16x32_bf16 v[32:35], v[236:239], v[128:131], v[32:35]
	v_mfma_f32_16x16x32_bf16 v[36:39], v[236:239], v[132:135], v[36:39]
	v_mfma_f32_16x16x32_bf16 v[40:43], v[240:243], v[128:131], v[40:43]
	v_mfma_f32_16x16x32_bf16 v[44:47], v[240:243], v[132:135], v[44:47]
	v_mfma_f32_16x16x32_bf16 v[48:51], v[244:247], v[128:131], v[48:51]
	v_mfma_f32_16x16x32_bf16 v[52:55], v[244:247], v[132:135], v[52:55]
	v_mfma_f32_16x16x32_bf16 v[56:59], v[248:251], v[128:131], v[56:59]
	v_mfma_f32_16x16x32_bf16 v[60:63], v[248:251], v[132:135], v[60:63]
	s_waitcnt lgkmcnt(7)
	v_mfma_f32_16x16x32_bf16 v[124:127], v[116:119], v[136:139], v[124:127]
	s_add_i32 s3, s3, 2
	v_pk_mul_f32 v[2:3], v[96:97], v[2:3]
	v_pk_mul_f32 v[0:1], v[98:99], v[0:1]
	v_mfma_f32_16x16x32_bf16 v[66:69], v[120:123], v[136:139], v[66:69]
	v_mul_f32_e64 v6, v96, v6
	v_mul_f32_e64 v7, v97, v7
	v_pk_mul_f32 v[4:5], v[98:99], v[4:5]
	v_pk_mul_f32 v[10:11], v[96:97], v[10:11]
	s_waitcnt lgkmcnt(5)
	v_mfma_f32_16x16x32_bf16 v[102:105], v[116:119], v[144:147], v[104:107]
	v_mul_f32_e64 v8, v98, v8
	v_mul_f32_e64 v9, v99, v9
	v_pk_mul_f32 v[14:15], v[96:97], v[14:15]
	v_pk_mul_f32 v[12:13], v[98:99], v[12:13]
	v_mfma_f32_16x16x32_bf16 v[74:77], v[120:123], v[144:147], v[74:77]
	v_mul_f32_e64 v18, v96, v18
	v_mul_f32_e64 v19, v97, v19
	v_pk_mul_f32 v[16:17], v[98:99], v[16:17]
	v_pk_mul_f32 v[22:23], v[96:97], v[22:23]
	s_waitcnt lgkmcnt(3)
	v_mfma_f32_16x16x32_bf16 v[106:109], v[116:119], v[152:155], v[108:111]
	v_mul_f32_e64 v20, v98, v20
	v_mul_f32_e64 v21, v99, v21
	v_pk_mul_f32 v[26:27], v[96:97], v[26:27]
	v_pk_mul_f32 v[24:25], v[98:99], v[24:25]
	v_mfma_f32_16x16x32_bf16 v[82:85], v[120:123], v[152:155], v[82:85]
	v_mul_f32_e64 v30, v96, v30
	v_mul_f32_e64 v31, v97, v31
	v_pk_mul_f32 v[28:29], v[98:99], v[28:29]
	v_pk_mul_f32 v[34:35], v[96:97], v[34:35]
	s_waitcnt lgkmcnt(1)
	v_mfma_f32_16x16x32_bf16 v[110:113], v[116:119], v[160:163], v[112:115]
	v_mul_f32_e64 v32, v98, v32
	v_mul_f32_e64 v33, v99, v33
	v_pk_mul_f32 v[38:39], v[96:97], v[38:39]
	v_pk_mul_f32 v[36:37], v[98:99], v[36:37]
	v_mfma_f32_16x16x32_bf16 v[86:89], v[120:123], v[160:163], v[86:89]
	v_mul_f32_e64 v42, v96, v42
	v_mul_f32_e64 v43, v97, v43
	v_pk_mul_f32 v[40:41], v[98:99], v[40:41]
	v_pk_mul_f32 v[46:47], v[96:97], v[46:47]
	v_mfma_f32_16x16x32_bf16 v[114:117], v[128:131], v[140:143], v[124:127]
	v_mul_f32_e64 v44, v98, v44
	v_mul_f32_e64 v45, v99, v45
	v_pk_mul_f32 v[50:51], v[96:97], v[50:51]
	v_pk_mul_f32 v[48:49], v[98:99], v[48:49]
	v_mfma_f32_16x16x32_bf16 v[66:69], v[132:135], v[140:143], v[66:69]
	v_mul_f32_e64 v54, v96, v54
	v_mul_f32_e64 v55, v97, v55
	s_nop 0
	v_cvt_pk_bf16_f32 v70, v114, v115
	v_cvt_pk_bf16_f32 v71, v116, v117
	v_mfma_f32_16x16x32_bf16 v[102:105], v[128:131], v[148:151], v[102:105]
	v_mul_f32_e64 v52, v98, v52
	v_mul_f32_e64 v53, v99, v53
	v_cvt_pk_bf16_f32 v66, v66, v67
	v_cvt_pk_bf16_f32 v67, v68, v69
	v_mfma_f32_16x16x32_bf16 v[74:77], v[132:135], v[148:151], v[74:77]
	ds_write2_b64 v92, v[70:71], v[66:67] offset1:4
	s_nop 1
	v_cvt_pk_bf16_f32 v66, v102, v103
	v_cvt_pk_bf16_f32 v67, v104, v105
	v_mfma_f32_16x16x32_bf16 v[106:109], v[128:131], v[156:159], v[106:109]
	v_mul_f32_e64 v58, v96, v58
	v_mul_f32_e64 v59, v97, v59
	v_cvt_pk_bf16_f32 v68, v74, v75
	v_cvt_pk_bf16_f32 v69, v76, v77
	v_mfma_f32_16x16x32_bf16 v[82:85], v[132:135], v[156:159], v[82:85]
	ds_write2_b64 v80, v[66:67], v[68:69] offset0:32 offset1:36
	s_nop 1
	v_cvt_pk_bf16_f32 v66, v106, v107
	v_cvt_pk_bf16_f32 v67, v108, v109
	s_waitcnt lgkmcnt(2)
	v_mfma_f32_16x16x32_bf16 v[110:113], v[128:131], v[164:167], v[110:113]
	v_mul_f32_e64 v56, v98, v56
	v_mul_f32_e64 v57, v99, v57
	v_cvt_pk_bf16_f32 v68, v82, v83
	v_cvt_pk_bf16_f32 v69, v84, v85
	v_mfma_f32_16x16x32_bf16 v[86:89], v[132:135], v[164:167], v[86:89]
	v_mul_f32_e64 v62, v96, v62
	v_mul_f32_e64 v63, v97, v63
	v_pk_mul_f32 v[60:61], v[98:99], v[60:61]
	ds_write2_b64 v72, v[66:67], v[68:69] offset0:64 offset1:68
	v_cvt_pk_bf16_f32 v66, v110, v111
	v_cvt_pk_bf16_f32 v67, v112, v113
	s_nop 1
	v_cvt_pk_bf16_f32 v68, v86, v87
	v_cvt_pk_bf16_f32 v69, v88, v89
	s_cmpk_lt_u32 s3, 0x42
	ds_write2_b64 v64, v[66:67], v[68:69] offset0:96 offset1:100
	s_waitcnt lgkmcnt(0)
	s_barrier
	s_cbranch_scc1 .LBB0_418
	s_setprio 0
	s_mov_b64 s[52:53], 0

.LBB0_440:
	s_setprio 2
	v_add_u32_e32 v118, v192, v193
	v_add_u32_e32 v117, v203, v202
	ds_read_b128 v[64:67], v118
	ds_read_b128 v[68:71], v118 offset:64
	ds_read_b128 v[72:75], v117 offset:34816
	ds_read_b128 v[76:79], v117 offset:34880
	ds_read_b128 v[80:83], v117 offset:39168
	ds_read_b128 v[84:87], v117 offset:39232
	ds_read_b128 v[88:91], v117 offset:43520
	ds_read_b128 v[92:95], v117 offset:43584
	ds_read_b128 v[96:99], v117 offset:47872
	ds_read_b128 v[100:103], v117 offset:47936
	ds_read_b128 v[104:107], v118 offset:128
	ds_read_b128 v[108:111], v118 offset:192
	ds_read_b128 v[112:115], v117 offset:34944
	ds_read_b128 v[120:123], v117 offset:35008
	ds_read_b128 v[124:127], v117 offset:39296
	ds_read_b128 v[128:131], v117 offset:39360
	ds_read_b128 v[132:135], v117 offset:43648
	ds_read_b128 v[136:139], v117 offset:43712
	ds_read_b128 v[140:143], v117 offset:48000
	ds_read_b128 v[144:147], v117 offset:48064
	s_waitcnt lgkmcnt(14)
	v_mfma_f32_16x16x32_bf16 v[72:75], v[72:75], v[64:67], 0
	v_mfma_f32_16x16x32_bf16 v[72:75], v[76:79], v[68:71], v[72:75]
	v_mfma_f32_16x16x32_bf16 v[80:83], v[80:83], v[64:67], 0
	s_waitcnt lgkmcnt(7)
	v_mfma_f32_16x16x32_bf16 v[72:75], v[112:115], v[104:107], v[72:75]
	v_mfma_f32_16x16x32_bf16 v[76:79], v[84:87], v[68:71], v[80:83]
	s_waitcnt lgkmcnt(6)
	v_mfma_f32_16x16x32_bf16 v[72:75], v[120:123], v[108:111], v[72:75]
	v_add_u32_e32 v120, v195, v196
	v_add_u32_e32 v121, v195, v205
	v_add_u32_e32 v122, v195, v207
	v_mfma_f32_16x16x32_bf16 v[88:91], v[88:91], v[64:67], 0
	v_add_u32_e32 v123, v195, v209
	s_nop 2
	v_cndmask_b32_e32 v72, 0, v72, vcc
	v_cndmask_b32_e64 v73, 0, v73, s[52:53]
	v_mfma_f32_16x16x32_bf16 v[64:67], v[96:99], v[64:67], 0
	v_cndmask_b32_e64 v74, 0, v74, s[54:55]
	v_cndmask_b32_e64 v75, 0, v75, s[56:57]
	v_cvt_pk_bf16_f32 v80, v72, v73
	s_waitcnt lgkmcnt(5)
	v_mfma_f32_16x16x32_bf16 v[76:79], v[124:127], v[104:107], v[76:79]
	v_cvt_pk_bf16_f32 v81, v74, v75
	ds_write_b64 v120, v[80:81]
	s_waitcnt lgkmcnt(5)
	v_mfma_f32_16x16x32_bf16 v[72:75], v[128:131], v[108:111], v[76:79]
	v_mfma_f32_16x16x32_bf16 v[76:79], v[92:95], v[68:71], v[88:91]
	v_mfma_f32_16x16x32_bf16 v[64:67], v[100:103], v[68:71], v[64:67]
	s_nop 5
	v_cndmask_b32_e64 v80, 0, v72, s[58:59]
	v_cndmask_b32_e64 v81, 0, v73, s[60:61]
	v_cndmask_b32_e64 v82, 0, v74, s[62:63]
	v_cndmask_b32_e64 v83, 0, v75, s[64:65]
	s_waitcnt lgkmcnt(4)
	v_mfma_f32_16x16x32_bf16 v[72:75], v[132:135], v[104:107], v[76:79]
	s_waitcnt lgkmcnt(2)
	v_mfma_f32_16x16x32_bf16 v[64:67], v[140:143], v[104:107], v[64:67]
	s_nop 0
	v_cvt_pk_bf16_f32 v76, v80, v81
	v_cvt_pk_bf16_f32 v77, v82, v83
	ds_write_b64 v121, v[76:77]
	v_mfma_f32_16x16x32_bf16 v[72:75], v[136:139], v[108:111], v[72:75]
	s_waitcnt lgkmcnt(2)
	v_mfma_f32_16x16x32_bf16 v[64:67], v[144:147], v[108:111], v[64:67]
	s_nop 5
	v_cndmask_b32_e64 v72, 0, v72, s[66:67]
	v_cndmask_b32_e64 v73, 0, v73, s[68:69]
	v_cndmask_b32_e64 v69, 0, v74, s[70:71]
	v_cndmask_b32_e64 v70, 0, v75, s[72:73]
	v_cndmask_b32_e64 v64, 0, v64, s[74:75]
	v_cndmask_b32_e64 v65, 0, v65, s[76:77]
	v_cndmask_b32_e64 v66, 0, v66, s[78:79]
	v_cndmask_b32_e64 v67, 0, v67, s[80:81]
	v_cvt_pk_bf16_f32 v68, v72, v73
	v_cvt_pk_bf16_f32 v69, v69, v70
	v_cvt_pk_bf16_f32 v64, v64, v65
	v_cvt_pk_bf16_f32 v65, v66, v67
	ds_write_b64 v122, v[68:69]
	ds_write_b64 v123, v[64:65]
	v_add_u32_e32 v119, v197, v202
	v_add_u32_e32 v116, 0x1000, v119
	v_add_u32_e32 v128, 0x2000, v119
	v_add_u32_e32 v132, 0x3000, v119
	ds_read2_b64 v[64:67], v119 offset1:4
	ds_read2_b64 v[68:71], v116 offset0:32 offset1:36
	ds_read2_b64 v[72:75], v128 offset0:64 offset1:68
	ds_read2_b64 v[76:79], v132 offset0:96 offset1:100
	ds_read2_b64 v[80:83], v119 offset0:8 offset1:12
	ds_read2_b64 v[84:87], v116 offset0:40 offset1:44
	ds_read2_b64 v[88:91], v128 offset0:72 offset1:76
	ds_read2_b64 v[92:95], v132 offset0:104 offset1:108
	ds_read2_b64 v[96:99], v119 offset0:16 offset1:20
	ds_read2_b64 v[100:103], v116 offset0:48 offset1:52
	ds_read2_b64 v[104:107], v128 offset0:80 offset1:84
	ds_read2_b64 v[108:111], v132 offset0:112 offset1:116
	ds_read2_b64 v[112:115], v119 offset0:24 offset1:28
	ds_read2_b64 v[124:127], v116 offset0:56 offset1:60
	ds_read2_b64 v[128:131], v128 offset0:88 offset1:92
	ds_read2_b64 v[132:135], v132 offset0:120 offset1:124
	v_cvt_pk_bf16_f32 v136, v0, v1
	v_cvt_pk_bf16_f32 v137, v2, v3
	v_cvt_pk_bf16_f32 v138, v8, v9
	v_cvt_pk_bf16_f32 v139, v10, v11
	v_cvt_pk_bf16_f32 v140, v4, v5
	v_cvt_pk_bf16_f32 v141, v6, v7
	v_cvt_pk_bf16_f32 v142, v12, v13
	v_cvt_pk_bf16_f32 v143, v14, v15
	s_waitcnt lgkmcnt(14)
	v_mfma_f32_16x16x32_bf16 v[144:147], v[136:139], v[64:67], 0
	v_cvt_pk_bf16_f32 v156, v16, v17
	v_cvt_pk_bf16_f32 v157, v18, v19
	v_cvt_pk_bf16_f32 v158, v24, v25
	v_mfma_f32_16x16x32_bf16 v[64:67], v[140:143], v[64:67], 0
	v_cvt_pk_bf16_f32 v159, v26, v27
	v_mfma_f32_16x16x32_bf16 v[148:151], v[136:139], v[68:71], 0
	v_mfma_f32_16x16x32_bf16 v[68:71], v[140:143], v[68:71], 0
	s_waitcnt lgkmcnt(13)
	v_mfma_f32_16x16x32_bf16 v[152:155], v[136:139], v[72:75], 0
	v_mfma_f32_16x16x32_bf16 v[72:75], v[140:143], v[72:75], 0
	s_waitcnt lgkmcnt(12)
	v_mfma_f32_16x16x32_bf16 v[136:139], v[136:139], v[76:79], 0
	v_mfma_f32_16x16x32_bf16 v[76:79], v[140:143], v[76:79], 0
	v_cvt_pk_bf16_f32 v140, v20, v21
	v_cvt_pk_bf16_f32 v141, v22, v23
	v_cvt_pk_bf16_f32 v142, v28, v29
	v_cvt_pk_bf16_f32 v143, v30, v31
	s_waitcnt lgkmcnt(11)
	v_mfma_f32_16x16x32_bf16 v[144:147], v[156:159], v[80:83], v[144:147]
	v_mfma_f32_16x16x32_bf16 v[64:67], v[140:143], v[80:83], v[64:67]
	s_waitcnt lgkmcnt(10)
	v_mfma_f32_16x16x32_bf16 v[80:83], v[156:159], v[84:87], v[148:151]
	v_mfma_f32_16x16x32_bf16 v[68:71], v[140:143], v[84:87], v[68:71]
	s_nop 1
	v_cvt_pk_bf16_f32 v148, v52, v53
	v_cvt_pk_bf16_f32 v149, v54, v55
	v_cvt_pk_bf16_f32 v150, v60, v61
	s_waitcnt lgkmcnt(9)
	v_mfma_f32_16x16x32_bf16 v[84:87], v[156:159], v[88:91], v[152:155]
	v_cvt_pk_bf16_f32 v151, v62, v63
	v_mfma_f32_16x16x32_bf16 v[72:75], v[140:143], v[88:91], v[72:75]
	s_waitcnt lgkmcnt(8)
	v_mfma_f32_16x16x32_bf16 v[88:91], v[156:159], v[92:95], v[136:139]
	s_nop 2
	v_cvt_pk_bf16_f32 v136, v32, v33
	v_cvt_pk_bf16_f32 v137, v34, v35
	v_cvt_pk_bf16_f32 v138, v40, v41
	v_cvt_pk_bf16_f32 v139, v42, v43
	v_mfma_f32_16x16x32_bf16 v[76:79], v[140:143], v[92:95], v[76:79]
	v_cvt_pk_bf16_f32 v92, v36, v37
	v_cvt_pk_bf16_f32 v93, v38, v39
	v_cvt_pk_bf16_f32 v94, v44, v45
	v_cvt_pk_bf16_f32 v95, v46, v47
	s_waitcnt lgkmcnt(7)
	v_mfma_f32_16x16x32_bf16 v[140:143], v[136:139], v[96:99], v[144:147]
	s_nop 2
	v_cvt_pk_bf16_f32 v144, v48, v49
	v_cvt_pk_bf16_f32 v145, v50, v51
	v_cvt_pk_bf16_f32 v146, v56, v57
	v_cvt_pk_bf16_f32 v147, v58, v59
	v_mfma_f32_16x16x32_bf16 v[64:67], v[92:95], v[96:99], v[64:67]
	s_waitcnt lgkmcnt(6)
	v_mfma_f32_16x16x32_bf16 v[80:83], v[136:139], v[100:103], v[80:83]
	v_mfma_f32_16x16x32_bf16 v[68:71], v[92:95], v[100:103], v[68:71]
	s_waitcnt lgkmcnt(5)
	v_mfma_f32_16x16x32_bf16 v[84:87], v[136:139], v[104:107], v[84:87]
	v_mfma_f32_16x16x32_bf16 v[72:75], v[92:95], v[104:107], v[72:75]
	s_waitcnt lgkmcnt(4)
	v_mfma_f32_16x16x32_bf16 v[136:139], v[136:139], v[108:111], v[88:91]
	v_mfma_f32_16x16x32_bf16 v[76:79], v[92:95], v[108:111], v[76:79]
	s_waitcnt lgkmcnt(3)
	v_mfma_f32_16x16x32_bf16 v[108:111], v[144:147], v[112:115], v[140:143]
	v_mfma_f32_16x16x32_bf16 v[104:107], v[148:151], v[112:115], v[64:67]
	s_waitcnt lgkmcnt(2)
	v_mfma_f32_16x16x32_bf16 v[100:103], v[144:147], v[124:127], v[80:83]
	v_mfma_f32_16x16x32_bf16 v[96:99], v[148:151], v[124:127], v[68:71]
	s_waitcnt lgkmcnt(1)
	v_mfma_f32_16x16x32_bf16 v[92:95], v[144:147], v[128:131], v[84:87]
	v_mfma_f32_16x16x32_bf16 v[88:91], v[148:151], v[128:131], v[72:75]
	s_waitcnt lgkmcnt(0)
	v_mfma_f32_16x16x32_bf16 v[80:83], v[144:147], v[132:135], v[136:139]
	v_mfma_f32_16x16x32_bf16 v[72:75], v[148:151], v[132:135], v[76:79]
	v_add_u32_e32 v68, v198, v210
	ds_read_b64_tr_b16 v[86:87], v68 offset:1088
	ds_read_b64_tr_b16 v[84:85], v68
	ds_read_b64_tr_b16 v[78:79], v68 offset:1120
	ds_read_b64_tr_b16 v[76:77], v68 offset:32
	ds_read_b64_tr_b16 v[64:65], v68 offset:8704
	ds_read_b64_tr_b16 v[66:67], v68 offset:9792
	ds_read_b64_tr_b16 v[70:71], v68 offset:9824
	ds_read_b64_tr_b16 v[68:69], v68 offset:8736
	ds_read_b64_tr_b16 v[112:113], v211 offset:34816
	ds_read_b64_tr_b16 v[124:125], v211 offset:34848
	ds_read_b64_tr_b16 v[128:129], v211 offset:34880
	ds_read_b64_tr_b16 v[132:133], v211 offset:34912
	ds_read_b64_tr_b16 v[114:115], v211 offset:35904
	ds_read_b64_tr_b16 v[126:127], v211 offset:35936
	ds_read_b64_tr_b16 v[130:131], v211 offset:35968
	ds_read_b64_tr_b16 v[134:135], v211 offset:36000
	ds_read_b64_tr_b16 v[136:137], v211 offset:34944
	ds_read_b64_tr_b16 v[140:141], v211 offset:34976
	ds_read_b64_tr_b16 v[144:145], v211 offset:35008
	ds_read_b64_tr_b16 v[148:149], v211 offset:35040
	ds_read_b64_tr_b16 v[138:139], v211 offset:36032
	ds_read_b64_tr_b16 v[142:143], v211 offset:36064
	ds_read_b64_tr_b16 v[146:147], v211 offset:36096
	ds_read_b64_tr_b16 v[150:151], v211 offset:36128
	ds_read_b64_tr_b16 v[152:153], v211 offset:43520
	ds_read_b64_tr_b16 v[156:157], v211 offset:43552
	ds_read_b64_tr_b16 v[160:161], v211 offset:43584
	ds_read_b64_tr_b16 v[164:165], v211 offset:43616
	ds_read_b64_tr_b16 v[154:155], v211 offset:44608
	ds_read_b64_tr_b16 v[158:159], v211 offset:44640
	ds_read_b64_tr_b16 v[162:163], v211 offset:44672
	ds_read_b64_tr_b16 v[166:167], v211 offset:44704
	ds_read_b64_tr_b16 v[168:169], v211 offset:43648
	ds_read_b64_tr_b16 v[182:183], v211 offset:43680
	ds_read_b64_tr_b16 v[186:187], v211 offset:43712
	ds_read_b64_tr_b16 v[232:233], v211 offset:43744
	ds_read_b64_tr_b16 v[170:171], v211 offset:44736
	ds_read_b64_tr_b16 v[184:185], v211 offset:44768
	ds_read_b64_tr_b16 v[188:189], v211 offset:44800
	ds_read_b64_tr_b16 v[234:235], v211 offset:44832
	s_waitcnt lgkmcnt(14)
	v_mfma_f32_16x16x32_bf16 v[0:3], v[112:115], v[84:87], v[0:3]
	v_add_u32_e32 v116, v199, v212
	s_waitcnt lgkmcnt(0)
	s_barrier
	v_mfma_f32_16x16x32_bf16 v[4:7], v[112:115], v[76:79], v[4:7]
	v_add_u32_e32 v112, 0x1bc00, v203
	v_mfma_f32_16x16x32_bf16 v[8:11], v[124:127], v[84:87], v[8:11]
	v_mfma_f32_16x16x32_bf16 v[12:15], v[124:127], v[76:79], v[12:15]
	v_mfma_f32_16x16x32_bf16 v[16:19], v[128:131], v[84:87], v[16:19]
	v_mfma_f32_16x16x32_bf16 v[20:23], v[128:131], v[76:79], v[20:23]
	v_mfma_f32_16x16x32_bf16 v[24:27], v[132:135], v[84:87], v[24:27]
	v_mfma_f32_16x16x32_bf16 v[28:31], v[132:135], v[76:79], v[28:31]
	v_mfma_f32_16x16x32_bf16 v[32:35], v[136:139], v[84:87], v[32:35]
	v_mfma_f32_16x16x32_bf16 v[36:39], v[136:139], v[76:79], v[36:39]
	v_mfma_f32_16x16x32_bf16 v[40:43], v[140:143], v[84:87], v[40:43]
	v_mfma_f32_16x16x32_bf16 v[44:47], v[140:143], v[76:79], v[44:47]
	v_mfma_f32_16x16x32_bf16 v[48:51], v[144:147], v[84:87], v[48:51]
	v_mfma_f32_16x16x32_bf16 v[52:55], v[144:147], v[76:79], v[52:55]
	v_mfma_f32_16x16x32_bf16 v[56:59], v[148:151], v[84:87], v[56:59]
	v_mfma_f32_16x16x32_bf16 v[60:63], v[148:151], v[76:79], v[60:63]
	v_mfma_f32_16x16x32_bf16 v[0:3], v[152:155], v[64:67], v[0:3]
	v_mfma_f32_16x16x32_bf16 v[4:7], v[152:155], v[68:71], v[4:7]
	ds_read_b128 v[124:127], v116
	ds_read_b128 v[128:131], v116 offset:2304
	ds_read_b128 v[132:135], v116 offset:4608
	ds_read_b128 v[136:139], v116 offset:6912
	ds_read_b128 v[140:143], v116 offset:64
	ds_read_b128 v[144:147], v116 offset:2368
	ds_read_b128 v[148:151], v116 offset:4672
	ds_read_b128 v[152:155], v116 offset:6976
	v_mfma_f32_16x16x32_bf16 v[8:11], v[156:159], v[64:67], v[8:11]
	v_mfma_f32_16x16x32_bf16 v[12:15], v[156:159], v[68:71], v[12:15]
	v_mfma_f32_16x16x32_bf16 v[16:19], v[160:163], v[64:67], v[16:19]
	v_mfma_f32_16x16x32_bf16 v[20:23], v[160:163], v[68:71], v[20:23]
	v_mfma_f32_16x16x32_bf16 v[24:27], v[164:167], v[64:67], v[24:27]
	v_mfma_f32_16x16x32_bf16 v[28:31], v[164:167], v[68:71], v[28:31]
	v_mfma_f32_16x16x32_bf16 v[32:35], v[168:171], v[64:67], v[32:35]
	v_mfma_f32_16x16x32_bf16 v[36:39], v[168:171], v[68:71], v[36:39]
	v_mfma_f32_16x16x32_bf16 v[40:43], v[182:185], v[64:67], v[40:43]
	v_mfma_f32_16x16x32_bf16 v[44:47], v[182:185], v[68:71], v[44:47]
	v_mfma_f32_16x16x32_bf16 v[48:51], v[186:189], v[64:67], v[48:51]
	v_mfma_f32_16x16x32_bf16 v[52:55], v[186:189], v[68:71], v[52:55]
	v_mfma_f32_16x16x32_bf16 v[56:59], v[232:235], v[64:67], v[56:59]
	v_mfma_f32_16x16x32_bf16 v[60:63], v[232:235], v[68:71], v[60:63]
	ds_read_b128 v[156:159], v112
	ds_read_b128 v[160:163], v112 offset:64
	ds_read_b128 v[164:167], v112 offset:128
	ds_read_b128 v[168:171], v112 offset:192
	ds_read_b128 v[182:185], v112 offset:256
	ds_read_b128 v[186:189], v112 offset:320
	ds_read_b128 v[232:235], v112 offset:384
	ds_read_b128 v[112:115], v112 offset:448
	s_waitcnt lgkmcnt(14)
	v_mfma_f32_16x16x32_bf16 v[108:111], v[84:87], v[124:127], v[108:111]
	s_waitcnt lgkmcnt(7)
	v_pk_mul_f32 v[2:3], v[2:3], v[158:159]
	v_pk_mul_f32 v[0:1], v[0:1], v[156:157]
	v_pk_mul_f32 v[6:7], v[6:7], v[158:159]
	v_mfma_f32_16x16x32_bf16 v[104:107], v[76:79], v[124:127], v[104:107]
	v_add_u32_e32 v124, v200, v202
	v_add_u32_e32 v125, 0x1000, v124
	v_add_u32_e32 v126, 0x2000, v124
	v_mfma_f32_16x16x32_bf16 v[100:103], v[84:87], v[128:131], v[100:103]
	v_add_u32_e32 v127, 0x3000, v124
	v_pk_mul_f32 v[4:5], v[4:5], v[156:157]
	s_waitcnt lgkmcnt(6)
	v_pk_mul_f32 v[10:11], v[10:11], v[162:163]
	v_mfma_f32_16x16x32_bf16 v[96:99], v[76:79], v[128:131], v[96:99]
	v_mul_f32_e64 v8, v8, v160
	v_mul_f32_e64 v9, v9, v161
	v_pk_mul_f32 v[14:15], v[14:15], v[162:163]
	v_pk_mul_f32 v[12:13], v[12:13], v[160:161]
	v_mfma_f32_16x16x32_bf16 v[92:95], v[84:87], v[132:135], v[92:95]
	s_waitcnt lgkmcnt(5)
	v_pk_mul_f32 v[18:19], v[18:19], v[166:167]
	v_pk_mul_f32 v[16:17], v[16:17], v[164:165]
	v_pk_mul_f32 v[22:23], v[22:23], v[166:167]
	v_mfma_f32_16x16x32_bf16 v[88:91], v[76:79], v[132:135], v[88:91]
	v_mul_f32_e64 v20, v20, v164
	v_mul_f32_e64 v21, v21, v165
	s_waitcnt lgkmcnt(4)
	v_pk_mul_f32 v[26:27], v[26:27], v[170:171]
	v_pk_mul_f32 v[24:25], v[24:25], v[168:169]
	v_mfma_f32_16x16x32_bf16 v[80:83], v[84:87], v[136:139], v[80:83]
	v_mul_f32_e64 v30, v30, v170
	v_mul_f32_e64 v31, v31, v171
	v_pk_mul_f32 v[28:29], v[28:29], v[168:169]
	s_waitcnt lgkmcnt(3)
	v_pk_mul_f32 v[34:35], v[34:35], v[184:185]
	v_mfma_f32_16x16x32_bf16 v[72:75], v[76:79], v[136:139], v[72:75]
	v_mul_f32_e64 v32, v32, v182
	v_mul_f32_e64 v33, v33, v183
	v_pk_mul_f32 v[38:39], v[38:39], v[184:185]
	v_pk_mul_f32 v[36:37], v[36:37], v[182:183]
	v_mfma_f32_16x16x32_bf16 v[76:79], v[64:67], v[140:143], v[108:111]
	s_waitcnt lgkmcnt(2)
	v_pk_mul_f32 v[42:43], v[42:43], v[188:189]
	v_pk_mul_f32 v[40:41], v[40:41], v[186:187]
	v_pk_mul_f32 v[46:47], v[46:47], v[188:189]
	v_mfma_f32_16x16x32_bf16 v[84:87], v[68:71], v[140:143], v[104:107]
	v_mul_f32_e64 v44, v44, v186
	v_mul_f32_e64 v45, v45, v187
	s_nop 0
	v_cvt_pk_bf16_f32 v108, v76, v77
	v_cvt_pk_bf16_f32 v109, v78, v79
	v_mfma_f32_16x16x32_bf16 v[76:79], v[64:67], v[144:147], v[100:103]
	s_waitcnt lgkmcnt(1)
	v_pk_mul_f32 v[50:51], v[50:51], v[234:235]
	v_cvt_pk_bf16_f32 v84, v84, v85
	v_cvt_pk_bf16_f32 v85, v86, v87
	ds_write2_b64 v124, v[108:109], v[84:85] offset1:4
	v_mfma_f32_16x16x32_bf16 v[84:87], v[68:71], v[144:147], v[96:99]
	s_nop 1
	v_cvt_pk_bf16_f32 v100, v76, v77
	v_cvt_pk_bf16_f32 v101, v78, v79
	v_pk_mul_f32 v[48:49], v[48:49], v[232:233]
	v_mfma_f32_16x16x32_bf16 v[76:79], v[64:67], v[148:151], v[92:95]
	v_mul_f32_e64 v54, v54, v234
	v_mul_f32_e64 v55, v55, v235
	v_cvt_pk_bf16_f32 v84, v84, v85
	v_cvt_pk_bf16_f32 v85, v86, v87
	ds_write2_b64 v125, v[100:101], v[84:85] offset0:32 offset1:36
	v_mfma_f32_16x16x32_bf16 v[84:87], v[68:71], v[148:151], v[88:91]
	s_nop 1
	v_cvt_pk_bf16_f32 v76, v76, v77
	v_cvt_pk_bf16_f32 v77, v78, v79
	v_pk_mul_f32 v[52:53], v[52:53], v[232:233]
	v_mfma_f32_16x16x32_bf16 v[64:67], v[64:67], v[152:155], v[80:83]
	s_waitcnt lgkmcnt(2)
	v_pk_mul_f32 v[58:59], v[58:59], v[114:115]
	v_cvt_pk_bf16_f32 v78, v84, v85
	v_cvt_pk_bf16_f32 v79, v86, v87
	v_mfma_f32_16x16x32_bf16 v[68:71], v[68:71], v[152:155], v[72:75]
	ds_write2_b64 v126, v[76:77], v[78:79] offset0:64 offset1:68
	s_nop 1
	v_cvt_pk_bf16_f32 v64, v64, v65
	v_cvt_pk_bf16_f32 v65, v66, v67
	v_pk_mul_f32 v[56:57], v[56:57], v[112:113]
	v_pk_mul_f32 v[62:63], v[62:63], v[114:115]
	s_nop 0
	v_cvt_pk_bf16_f32 v66, v68, v69
	v_cvt_pk_bf16_f32 v67, v70, v71
	ds_write2_b64 v127, v[64:65], v[66:67] offset0:96 offset1:100
	s_waitcnt lgkmcnt(0)
	s_barrier
	ds_read_b128 v[64:67], v118 offset:17408
	ds_read_b128 v[68:71], v118 offset:17472
	ds_read_b128 v[72:75], v117 offset:52224
	ds_read_b128 v[76:79], v117 offset:52288
	ds_read_b128 v[80:83], v117 offset:56576
	ds_read_b128 v[84:87], v117 offset:56640
	ds_read_b128 v[88:91], v117 offset:60928
	ds_read_b128 v[92:95], v117 offset:60992
	ds_read_b128 v[96:99], v117 offset:65280
	ds_read_b128 v[100:103], v117 offset:65344
	ds_read_b128 v[104:107], v118 offset:17536
	ds_read_b128 v[108:111], v118 offset:17600
	ds_read_b128 v[128:131], v117 offset:52352
	ds_read_b128 v[132:135], v117 offset:52416
	ds_read_b128 v[136:139], v117 offset:56704
	ds_read_b128 v[140:143], v117 offset:56768
	ds_read_b128 v[144:147], v117 offset:61056
	ds_read_b128 v[148:151], v117 offset:61120
	ds_read_b128 v[152:155], v117 offset:65408
	ds_read_b128 v[156:159], v117 offset:65472
	v_pk_mul_f32 v[60:61], v[60:61], v[112:113]
	s_waitcnt lgkmcnt(14)
	v_mfma_f32_16x16x32_bf16 v[72:75], v[72:75], v[64:67], 0
	v_mfma_f32_16x16x32_bf16 v[72:75], v[76:79], v[68:71], v[72:75]
	v_mfma_f32_16x16x32_bf16 v[80:83], v[80:83], v[64:67], 0
	s_waitcnt lgkmcnt(7)
	v_mfma_f32_16x16x32_bf16 v[72:75], v[128:131], v[104:107], v[72:75]
	v_mfma_f32_16x16x32_bf16 v[76:79], v[84:87], v[68:71], v[80:83]
	v_mfma_f32_16x16x32_bf16 v[88:91], v[88:91], v[64:67], 0
	v_mfma_f32_16x16x32_bf16 v[64:67], v[96:99], v[64:67], 0
	s_waitcnt lgkmcnt(6)
	v_mfma_f32_16x16x32_bf16 v[72:75], v[132:135], v[108:111], v[72:75]
	s_waitcnt lgkmcnt(5)
	v_mfma_f32_16x16x32_bf16 v[76:79], v[136:139], v[104:107], v[76:79]
	v_mfma_f32_16x16x32_bf16 v[80:83], v[92:95], v[68:71], v[88:91]
	s_nop 4
	v_cndmask_b32_e32 v72, 0, v72, vcc
	v_cndmask_b32_e64 v73, 0, v73, s[52:53]
	v_cndmask_b32_e64 v74, 0, v74, s[54:55]
	v_mfma_f32_16x16x32_bf16 v[64:67], v[100:103], v[68:71], v[64:67]
	v_cndmask_b32_e64 v75, 0, v75, s[56:57]
	v_cvt_pk_bf16_f32 v84, v72, v73
	v_cvt_pk_bf16_f32 v85, v74, v75
	s_waitcnt lgkmcnt(4)
	v_mfma_f32_16x16x32_bf16 v[72:75], v[140:143], v[108:111], v[76:79]
	ds_write_b64 v120, v[84:85]
	s_waitcnt lgkmcnt(4)
	v_mfma_f32_16x16x32_bf16 v[76:79], v[144:147], v[104:107], v[80:83]
	s_waitcnt lgkmcnt(2)
	v_mfma_f32_16x16x32_bf16 v[64:67], v[152:155], v[104:107], v[64:67]
	s_nop 2
	v_cndmask_b32_e64 v72, 0, v72, s[58:59]
	v_cndmask_b32_e64 v73, 0, v73, s[60:61]
	v_cndmask_b32_e64 v81, 0, v74, s[62:63]
	v_cndmask_b32_e64 v82, 0, v75, s[64:65]
	v_cvt_pk_bf16_f32 v80, v72, v73
	v_mfma_f32_16x16x32_bf16 v[72:75], v[148:151], v[108:111], v[76:79]
	v_cvt_pk_bf16_f32 v81, v81, v82
	ds_write_b64 v121, v[80:81]
	s_waitcnt lgkmcnt(2)
	v_mfma_f32_16x16x32_bf16 v[64:67], v[156:159], v[108:111], v[64:67]
	s_nop 3
	v_cndmask_b32_e64 v72, 0, v72, s[66:67]
	v_cndmask_b32_e64 v68, 0, v73, s[68:69]
	v_cndmask_b32_e64 v69, 0, v74, s[70:71]
	v_cndmask_b32_e64 v70, 0, v75, s[72:73]
	v_cndmask_b32_e64 v64, 0, v64, s[74:75]
	v_cndmask_b32_e64 v65, 0, v65, s[76:77]
	v_cndmask_b32_e64 v66, 0, v66, s[78:79]
	v_cndmask_b32_e64 v67, 0, v67, s[80:81]
	v_cvt_pk_bf16_f32 v68, v72, v68
	v_cvt_pk_bf16_f32 v69, v69, v70
	v_cvt_pk_bf16_f32 v64, v64, v65
	v_cvt_pk_bf16_f32 v65, v66, v67
	ds_write_b64 v122, v[68:69]
	ds_write_b64 v123, v[64:65]
	v_add_u32_e32 v112, 0x4000, v119
	v_add_u32_e32 v117, 0x5000, v119
	v_add_u32_e32 v122, 0x6000, v119
	v_add_u32_e32 v123, 0x7000, v119
	ds_read2_b64 v[64:67], v112 offset0:128 offset1:132
	ds_read2_b64 v[68:71], v117 offset0:160 offset1:164
	ds_read2_b64 v[72:75], v122 offset0:192 offset1:196
	ds_read2_b64 v[76:79], v123 offset0:224 offset1:228
	ds_read2_b64 v[80:83], v112 offset0:136 offset1:140
	ds_read2_b64 v[84:87], v117 offset0:168 offset1:172
	ds_read2_b64 v[88:91], v122 offset0:200 offset1:204
	ds_read2_b64 v[92:95], v123 offset0:232 offset1:236
	ds_read2_b64 v[96:99], v112 offset0:144 offset1:148
	ds_read2_b64 v[100:103], v117 offset0:176 offset1:180
	ds_read2_b64 v[104:107], v122 offset0:208 offset1:212
	ds_read2_b64 v[108:111], v123 offset0:240 offset1:244
	ds_read2_b64 v[112:115], v112 offset0:152 offset1:156
	ds_read2_b64 v[118:121], v117 offset0:184 offset1:188
	ds_read2_b64 v[128:131], v122 offset0:216 offset1:220
	ds_read2_b64 v[132:135], v123 offset0:248 offset1:252
	v_cvt_pk_bf16_f32 v136, v0, v1
	v_cvt_pk_bf16_f32 v137, v2, v3
	v_cvt_pk_bf16_f32 v138, v8, v9
	v_cvt_pk_bf16_f32 v139, v10, v11
	v_cvt_pk_bf16_f32 v140, v4, v5
	v_cvt_pk_bf16_f32 v141, v6, v7
	v_cvt_pk_bf16_f32 v142, v12, v13
	v_cvt_pk_bf16_f32 v143, v14, v15
	s_waitcnt lgkmcnt(14)
	v_mfma_f32_16x16x32_bf16 v[144:147], v[136:139], v[64:67], 0
	v_cvt_pk_bf16_f32 v156, v16, v17
	v_cvt_pk_bf16_f32 v157, v18, v19
	v_cvt_pk_bf16_f32 v158, v24, v25
	v_mfma_f32_16x16x32_bf16 v[64:67], v[140:143], v[64:67], 0
	v_cvt_pk_bf16_f32 v159, v26, v27
	v_mfma_f32_16x16x32_bf16 v[148:151], v[136:139], v[68:71], 0
	v_mfma_f32_16x16x32_bf16 v[68:71], v[140:143], v[68:71], 0
	s_waitcnt lgkmcnt(13)
	v_mfma_f32_16x16x32_bf16 v[152:155], v[136:139], v[72:75], 0
	v_mfma_f32_16x16x32_bf16 v[72:75], v[140:143], v[72:75], 0
	s_waitcnt lgkmcnt(12)
	v_mfma_f32_16x16x32_bf16 v[136:139], v[136:139], v[76:79], 0
	v_mfma_f32_16x16x32_bf16 v[76:79], v[140:143], v[76:79], 0
	v_cvt_pk_bf16_f32 v140, v20, v21
	v_cvt_pk_bf16_f32 v141, v22, v23
	v_cvt_pk_bf16_f32 v142, v28, v29
	v_cvt_pk_bf16_f32 v143, v30, v31
	s_waitcnt lgkmcnt(11)
	v_mfma_f32_16x16x32_bf16 v[144:147], v[156:159], v[80:83], v[144:147]
	v_mfma_f32_16x16x32_bf16 v[64:67], v[140:143], v[80:83], v[64:67]
	s_waitcnt lgkmcnt(10)
	v_mfma_f32_16x16x32_bf16 v[80:83], v[156:159], v[84:87], v[148:151]
	v_mfma_f32_16x16x32_bf16 v[68:71], v[140:143], v[84:87], v[68:71]
	s_nop 1
	v_cvt_pk_bf16_f32 v148, v52, v53
	v_cvt_pk_bf16_f32 v149, v54, v55
	v_cvt_pk_bf16_f32 v150, v60, v61
	s_waitcnt lgkmcnt(9)
	v_mfma_f32_16x16x32_bf16 v[84:87], v[156:159], v[88:91], v[152:155]
	v_cvt_pk_bf16_f32 v151, v62, v63
	v_mfma_f32_16x16x32_bf16 v[72:75], v[140:143], v[88:91], v[72:75]
	s_waitcnt lgkmcnt(8)
	v_mfma_f32_16x16x32_bf16 v[88:91], v[156:159], v[92:95], v[136:139]
	s_nop 2
	v_cvt_pk_bf16_f32 v136, v32, v33
	v_cvt_pk_bf16_f32 v137, v34, v35
	v_cvt_pk_bf16_f32 v138, v40, v41
	v_cvt_pk_bf16_f32 v139, v42, v43
	v_mfma_f32_16x16x32_bf16 v[76:79], v[140:143], v[92:95], v[76:79]
	v_cvt_pk_bf16_f32 v92, v36, v37
	v_cvt_pk_bf16_f32 v93, v38, v39
	v_cvt_pk_bf16_f32 v94, v44, v45
	v_cvt_pk_bf16_f32 v95, v46, v47
	s_waitcnt lgkmcnt(7)
	v_mfma_f32_16x16x32_bf16 v[140:143], v[136:139], v[96:99], v[144:147]
	s_waitcnt lgkmcnt(6)
	v_mfma_f32_16x16x32_bf16 v[80:83], v[136:139], v[100:103], v[80:83]
	s_waitcnt lgkmcnt(5)
	v_mfma_f32_16x16x32_bf16 v[84:87], v[136:139], v[104:107], v[84:87]
	s_waitcnt lgkmcnt(4)
	v_mfma_f32_16x16x32_bf16 v[88:91], v[136:139], v[108:111], v[88:91]
	v_cvt_pk_bf16_f32 v136, v48, v49
	v_cvt_pk_bf16_f32 v137, v50, v51
	v_cvt_pk_bf16_f32 v138, v56, v57
	v_cvt_pk_bf16_f32 v139, v58, v59
	v_mfma_f32_16x16x32_bf16 v[64:67], v[92:95], v[96:99], v[64:67]
	v_mfma_f32_16x16x32_bf16 v[68:71], v[92:95], v[100:103], v[68:71]
	v_mfma_f32_16x16x32_bf16 v[72:75], v[92:95], v[104:107], v[72:75]
	v_mfma_f32_16x16x32_bf16 v[144:147], v[92:95], v[108:111], v[76:79]
	s_waitcnt lgkmcnt(3)
	v_mfma_f32_16x16x32_bf16 v[108:111], v[136:139], v[112:115], v[140:143]
	v_mfma_f32_16x16x32_bf16 v[104:107], v[148:151], v[112:115], v[64:67]
	s_waitcnt lgkmcnt(2)
	v_mfma_f32_16x16x32_bf16 v[100:103], v[136:139], v[118:121], v[80:83]
	v_mfma_f32_16x16x32_bf16 v[96:99], v[148:151], v[118:121], v[68:71]
	s_waitcnt lgkmcnt(1)
	v_mfma_f32_16x16x32_bf16 v[92:95], v[136:139], v[128:131], v[84:87]
	v_mfma_f32_16x16x32_bf16 v[80:83], v[148:151], v[128:131], v[72:75]
	s_waitcnt lgkmcnt(0)
	v_mfma_f32_16x16x32_bf16 v[76:79], v[136:139], v[132:135], v[88:91]
	v_mfma_f32_16x16x32_bf16 v[72:75], v[148:151], v[132:135], v[144:147]
	v_add_u32_e32 v64, v201, v210
	s_nop 0
	ds_read_b64_tr_b16 v[90:91], v64 offset:1088
	ds_read_b64_tr_b16 v[88:89], v64
	ds_read_b64_tr_b16 v[86:87], v64 offset:1120
	ds_read_b64_tr_b16 v[84:85], v64 offset:32
	ds_read_b64_tr_b16 v[68:69], v64 offset:8704
	ds_read_b64_tr_b16 v[70:71], v64 offset:9792
	ds_read_b64_tr_b16 v[66:67], v64 offset:9824
	ds_read_b64_tr_b16 v[64:65], v64 offset:8736
	ds_read_b64_tr_b16 v[112:113], v211 offset:52224
	ds_read_b64_tr_b16 v[118:119], v211 offset:52256
	ds_read_b64_tr_b16 v[128:129], v211 offset:52288
	ds_read_b64_tr_b16 v[132:133], v211 offset:52320
	ds_read_b64_tr_b16 v[114:115], v211 offset:53312
	ds_read_b64_tr_b16 v[120:121], v211 offset:53344
	ds_read_b64_tr_b16 v[130:131], v211 offset:53376
	ds_read_b64_tr_b16 v[134:135], v211 offset:53408
	ds_read_b64_tr_b16 v[136:137], v211 offset:52352
	ds_read_b64_tr_b16 v[140:141], v211 offset:52384
	ds_read_b64_tr_b16 v[144:145], v211 offset:52416
	ds_read_b64_tr_b16 v[148:149], v211 offset:52448
	ds_read_b64_tr_b16 v[138:139], v211 offset:53440
	ds_read_b64_tr_b16 v[142:143], v211 offset:53472
	ds_read_b64_tr_b16 v[146:147], v211 offset:53504
	ds_read_b64_tr_b16 v[150:151], v211 offset:53536
	ds_read_b64_tr_b16 v[152:153], v211 offset:60928
	ds_read_b64_tr_b16 v[156:157], v211 offset:60960
	ds_read_b64_tr_b16 v[160:161], v211 offset:60992
	ds_read_b64_tr_b16 v[164:165], v211 offset:61024
	ds_read_b64_tr_b16 v[154:155], v211 offset:62016
	ds_read_b64_tr_b16 v[158:159], v211 offset:62048
	ds_read_b64_tr_b16 v[162:163], v211 offset:62080
	ds_read_b64_tr_b16 v[166:167], v211 offset:62112
	ds_read_b64_tr_b16 v[168:169], v211 offset:61056
	ds_read_b64_tr_b16 v[182:183], v211 offset:61088
	ds_read_b64_tr_b16 v[186:187], v211 offset:61120
	ds_read_b64_tr_b16 v[232:233], v211 offset:61152
	ds_read_b64_tr_b16 v[170:171], v211 offset:62144
	ds_read_b64_tr_b16 v[184:185], v211 offset:62176
	ds_read_b64_tr_b16 v[188:189], v211 offset:62208
	ds_read_b64_tr_b16 v[234:235], v211 offset:62240
	s_waitcnt lgkmcnt(14)
	v_mfma_f32_16x16x32_bf16 v[0:3], v[112:115], v[88:91], v[0:3]
	s_waitcnt lgkmcnt(0)
	s_barrier
	v_mfma_f32_16x16x32_bf16 v[4:7], v[112:115], v[84:87], v[4:7]
	v_mfma_f32_16x16x32_bf16 v[8:11], v[118:121], v[88:91], v[8:11]
	v_mfma_f32_16x16x32_bf16 v[12:15], v[118:121], v[84:87], v[12:15]
	v_mfma_f32_16x16x32_bf16 v[16:19], v[128:131], v[88:91], v[16:19]
	v_mfma_f32_16x16x32_bf16 v[20:23], v[128:131], v[84:87], v[20:23]
	v_mfma_f32_16x16x32_bf16 v[24:27], v[132:135], v[88:91], v[24:27]
	v_mfma_f32_16x16x32_bf16 v[28:31], v[132:135], v[84:87], v[28:31]
	v_mfma_f32_16x16x32_bf16 v[32:35], v[136:139], v[88:91], v[32:35]
	v_mfma_f32_16x16x32_bf16 v[36:39], v[136:139], v[84:87], v[36:39]
	v_mfma_f32_16x16x32_bf16 v[40:43], v[140:143], v[88:91], v[40:43]
	v_mfma_f32_16x16x32_bf16 v[44:47], v[140:143], v[84:87], v[44:47]
	v_mfma_f32_16x16x32_bf16 v[48:51], v[144:147], v[88:91], v[48:51]
	v_mfma_f32_16x16x32_bf16 v[52:55], v[144:147], v[84:87], v[52:55]
	v_mfma_f32_16x16x32_bf16 v[56:59], v[148:151], v[88:91], v[56:59]
	v_mfma_f32_16x16x32_bf16 v[60:63], v[148:151], v[84:87], v[60:63]
	ds_read_b128 v[112:115], v116
	ds_read_b128 v[118:121], v116 offset:2304
	ds_read_b128 v[128:131], v116 offset:4608
	ds_read_b128 v[132:135], v116 offset:6912
	ds_read_b128 v[136:139], v116 offset:64
	ds_read_b128 v[140:143], v116 offset:2368
	ds_read_b128 v[144:147], v116 offset:4672
	ds_read_b128 v[148:151], v116 offset:6976
	v_add_u32_e32 v116, 0x1be00, v203
	v_mfma_f32_16x16x32_bf16 v[0:3], v[152:155], v[68:71], v[0:3]
	v_mfma_f32_16x16x32_bf16 v[4:7], v[152:155], v[64:67], v[4:7]
	v_mfma_f32_16x16x32_bf16 v[8:11], v[156:159], v[68:71], v[8:11]
	v_mfma_f32_16x16x32_bf16 v[12:15], v[156:159], v[64:67], v[12:15]
	v_mfma_f32_16x16x32_bf16 v[16:19], v[160:163], v[68:71], v[16:19]
	v_mfma_f32_16x16x32_bf16 v[20:23], v[160:163], v[64:67], v[20:23]
	v_mfma_f32_16x16x32_bf16 v[24:27], v[164:167], v[68:71], v[24:27]
	v_mfma_f32_16x16x32_bf16 v[28:31], v[164:167], v[64:67], v[28:31]
	v_mfma_f32_16x16x32_bf16 v[32:35], v[168:171], v[68:71], v[32:35]
	v_mfma_f32_16x16x32_bf16 v[36:39], v[168:171], v[64:67], v[36:39]
	v_mfma_f32_16x16x32_bf16 v[40:43], v[182:185], v[68:71], v[40:43]
	v_mfma_f32_16x16x32_bf16 v[44:47], v[182:185], v[64:67], v[44:47]
	v_mfma_f32_16x16x32_bf16 v[48:51], v[186:189], v[68:71], v[48:51]
	v_mfma_f32_16x16x32_bf16 v[52:55], v[186:189], v[64:67], v[52:55]
	v_mfma_f32_16x16x32_bf16 v[56:59], v[232:235], v[68:71], v[56:59]
	v_mfma_f32_16x16x32_bf16 v[60:63], v[232:235], v[64:67], v[60:63]
	ds_read_b128 v[152:155], v116
	ds_read_b128 v[156:159], v116 offset:64
	ds_read_b128 v[160:163], v116 offset:128
	ds_read_b128 v[164:167], v116 offset:192
	ds_read_b128 v[168:171], v116 offset:256
	ds_read_b128 v[182:185], v116 offset:320
	ds_read_b128 v[186:189], v116 offset:384
	ds_read_b128 v[232:235], v116 offset:448
	s_waitcnt lgkmcnt(14)
	v_mfma_f32_16x16x32_bf16 v[108:111], v[88:91], v[112:115], v[108:111]
	s_add_i32 s2, s2, 2
	s_waitcnt lgkmcnt(7)
	v_pk_mul_f32 v[2:3], v[2:3], v[154:155]
	v_pk_mul_f32 v[0:1], v[0:1], v[152:153]
	v_mfma_f32_16x16x32_bf16 v[104:107], v[84:87], v[112:115], v[104:107]
	v_mul_f32_e64 v6, v6, v154
	v_mul_f32_e64 v7, v7, v155
	v_pk_mul_f32 v[4:5], v[4:5], v[152:153]
	s_waitcnt lgkmcnt(6)
	v_pk_mul_f32 v[10:11], v[10:11], v[158:159]
	v_mfma_f32_16x16x32_bf16 v[100:103], v[88:91], v[118:121], v[100:103]
	v_mul_f32_e64 v8, v8, v156
	v_mul_f32_e64 v9, v9, v157
	v_pk_mul_f32 v[14:15], v[14:15], v[158:159]
	v_pk_mul_f32 v[12:13], v[12:13], v[156:157]
	v_mfma_f32_16x16x32_bf16 v[96:99], v[84:87], v[118:121], v[96:99]
	s_waitcnt lgkmcnt(5)
	v_pk_mul_f32 v[18:19], v[18:19], v[162:163]
	v_pk_mul_f32 v[16:17], v[16:17], v[160:161]
	v_pk_mul_f32 v[22:23], v[22:23], v[162:163]
	v_mfma_f32_16x16x32_bf16 v[92:95], v[88:91], v[128:131], v[92:95]
	v_mul_f32_e64 v20, v20, v160
	v_mul_f32_e64 v21, v21, v161
	s_waitcnt lgkmcnt(4)
	v_pk_mul_f32 v[26:27], v[26:27], v[166:167]
	v_pk_mul_f32 v[24:25], v[24:25], v[164:165]
	v_mfma_f32_16x16x32_bf16 v[80:83], v[84:87], v[128:131], v[80:83]
	v_mul_f32_e64 v30, v30, v166
	v_mul_f32_e64 v31, v31, v167
	v_pk_mul_f32 v[28:29], v[28:29], v[164:165]
	s_waitcnt lgkmcnt(3)
	v_pk_mul_f32 v[34:35], v[34:35], v[170:171]
	v_mfma_f32_16x16x32_bf16 v[76:79], v[88:91], v[132:135], v[76:79]
	v_mul_f32_e64 v32, v32, v168
	v_mul_f32_e64 v33, v33, v169
	v_pk_mul_f32 v[38:39], v[38:39], v[170:171]
	v_pk_mul_f32 v[36:37], v[36:37], v[168:169]
	v_mfma_f32_16x16x32_bf16 v[72:75], v[84:87], v[132:135], v[72:75]
	s_waitcnt lgkmcnt(2)
	v_pk_mul_f32 v[42:43], v[42:43], v[184:185]
	v_pk_mul_f32 v[40:41], v[40:41], v[182:183]
	v_pk_mul_f32 v[46:47], v[46:47], v[184:185]
	v_mfma_f32_16x16x32_bf16 v[84:87], v[68:71], v[136:139], v[108:111]
	v_mul_f32_e64 v44, v44, v182
	v_mul_f32_e64 v45, v45, v183
	s_waitcnt lgkmcnt(1)
	v_pk_mul_f32 v[50:51], v[50:51], v[188:189]
	v_pk_mul_f32 v[48:49], v[48:49], v[186:187]
	v_mfma_f32_16x16x32_bf16 v[88:91], v[64:67], v[136:139], v[104:107]
	v_mul_f32_e64 v54, v54, v188
	v_mul_f32_e64 v55, v55, v189
	v_pk_mul_f32 v[52:53], v[52:53], v[186:187]
	s_waitcnt lgkmcnt(0)
	v_pk_mul_f32 v[58:59], v[58:59], v[234:235]
	v_mfma_f32_16x16x32_bf16 v[100:103], v[68:71], v[140:143], v[100:103]
	v_cvt_pk_bf16_f32 v104, v84, v85
	v_cvt_pk_bf16_f32 v105, v86, v87
	v_cvt_pk_bf16_f32 v88, v88, v89
	v_mfma_f32_16x16x32_bf16 v[84:87], v[64:67], v[140:143], v[96:99]
	v_cvt_pk_bf16_f32 v89, v90, v91
	ds_write2_b64 v124, v[104:105], v[88:89] offset1:4
	v_pk_mul_f32 v[56:57], v[56:57], v[232:233]
	v_mfma_f32_16x16x32_bf16 v[88:91], v[68:71], v[144:147], v[92:95]
	v_cvt_pk_bf16_f32 v96, v100, v101
	v_cvt_pk_bf16_f32 v97, v102, v103
	s_nop 1
	v_cvt_pk_bf16_f32 v84, v84, v85
	v_mfma_f32_16x16x32_bf16 v[80:83], v[64:67], v[144:147], v[80:83]
	v_cvt_pk_bf16_f32 v85, v86, v87
	v_pk_mul_f32 v[62:63], v[62:63], v[234:235]
	v_pk_mul_f32 v[60:61], v[60:61], v[232:233]
	v_mfma_f32_16x16x32_bf16 v[68:71], v[68:71], v[148:151], v[76:79]
	ds_write2_b64 v125, v[96:97], v[84:85] offset0:32 offset1:36
	v_cvt_pk_bf16_f32 v84, v88, v89
	v_cvt_pk_bf16_f32 v85, v90, v91
	v_mfma_f32_16x16x32_bf16 v[64:67], v[64:67], v[148:151], v[72:75]
	v_cvt_pk_bf16_f32 v76, v80, v81
	v_cvt_pk_bf16_f32 v77, v82, v83
	s_nop 1
	v_cvt_pk_bf16_f32 v68, v68, v69
	v_cvt_pk_bf16_f32 v69, v70, v71
	s_cmpk_lt_u32 s2, 0x42
	s_nop 0
	v_cvt_pk_bf16_f32 v64, v64, v65
	v_cvt_pk_bf16_f32 v65, v66, v67
	ds_write2_b64 v126, v[84:85], v[76:77] offset0:64 offset1:68
	ds_write2_b64 v127, v[68:69], v[64:65] offset0:96 offset1:100
	s_waitcnt lgkmcnt(0)
	s_barrier
	s_cbranch_scc1 .LBB0_440
	s_setprio 0
	s_mov_b64 s[52:53], 0

.LBB0_1753:
	s_add_i32 s59, s59, 1
	s_mul_i32 s2, s59, s60
	s_mul_hi_u32 s3, s59, s56
	s_add_i32 s3, s3, s2
	s_mul_i32 s2, s59, s56
	s_add_u32 s2, s2, s8
	s_addc_u32 s3, s3, s9
	v_cmp_ge_i64_e32 vcc, s[2:3], v[150:151]
	v_cmp_lt_i64_e64 s[4:5], s[2:3], v[150:151]
	s_cbranch_vccnz .LBB0_1755
	s_ashr_i32 s3, s2, 31
	s_lshr_b32 s3, s3, 29
	s_add_i32 s3, s2, s3
	s_ashr_i32 s26, s3, 3
	s_and_b32 s3, s3, -8
	s_sub_i32 s2, s2, s3
	s_cmp_lt_i32 s2, 0
	s_cselect_b32 s3, s53, s12
	s_mul_i32 s2, s3, s2
	s_add_i32 s2, s2, s26
	s_ashr_i32 s3, s2, 31
	s_lshr_b32 s3, s3, 26
	s_add_i32 s3, s2, s3
	s_ashr_i32 s26, s3, 6
	s_lshl_b32 s27, s26, 3
	s_sub_i32 s26, s12, s27
	s_min_i32 s28, s26, 8
	s_abs_i32 s26, s28
	v_cvt_f32_u32_e32 v0, s26
	s_sub_i32 s30, 0, s26
	s_andn2_b32 s3, s3, 63
	s_sub_i32 s2, s2, s3
	v_rcp_iflag_f32_e32 v0, v0
	s_abs_i32 s3, s2
	s_xor_b32 s29, s2, s28
	s_ashr_i32 s29, s29, 31
	v_mul_f32_e32 v0, 0x4f7ffffe, v0
	v_cvt_u32_f32_e32 v0, v0
	s_nop 0
	v_readfirstlane_b32 s31, v0
	s_mul_i32 s30, s30, s31
	s_mul_hi_u32 s30, s31, s30
	s_add_i32 s31, s31, s30
	s_mul_hi_u32 s30, s3, s31
	s_mul_i32 s31, s30, s26
	s_sub_i32 s3, s3, s31
	s_add_i32 s34, s30, 1
	s_sub_i32 s31, s3, s26
	s_cmp_ge_u32 s3, s26
	s_cselect_b32 s30, s34, s30
	s_cselect_b32 s3, s31, s3
	s_add_i32 s31, s30, 1
	s_cmp_ge_u32 s3, s26
	s_cselect_b32 s3, s31, s30
	s_xor_b32 s3, s3, s29
	s_sub_i32 s26, s3, s29
	s_mul_i32 s3, s26, s28
	s_sub_i32 s2, s2, s3
	s_add_i32 s28, s2, s27
	s_ashr_i32 s29, s28, 31
	s_lshl_b64 s[2:3], s[28:29], 2
	s_add_u32 s2, s50, s2
	s_addc_u32 s3, s51, s3
	global_load_dword v177, v145, s[2:3]
	s_lshl_b32 s27, s28, 8
	v_add_u32_e32 v0, s27, v162
	v_add_u32_e32 v2, s27, v163
	s_bitset1_b32 s27, 7
	v_ashrrev_i32_e32 v1, 31, v0
	v_ashrrev_i32_e32 v3, 31, v2
	v_add_u32_e32 v4, s27, v162
	v_add_u32_e32 v6, s27, v163
	v_lshl_add_u64 v[0:1], v[0:1], 2, s[16:17]
	v_lshl_add_u64 v[2:3], v[2:3], 2, s[16:17]
	v_ashrrev_i32_e32 v5, 31, v4
	v_ashrrev_i32_e32 v7, 31, v6
	v_lshl_add_u64 v[4:5], v[4:5], 2, s[16:17]
	v_lshl_add_u64 v[6:7], v[6:7], 2, s[16:17]
	global_load_dword v248, v[0:1], off
	s_nop 0
	global_load_dword v249, v[2:3], off
	s_nop 0
	global_load_dword v250, v[4:5], off
	global_load_dword v251, v[6:7], off
	s_waitcnt vmcnt(0)
	v_readfirstlane_b32 s2, v177
	s_ashr_i32 s3, s2, 31
	s_lshl_b64 s[2:3], s[2:3], 22
	s_add_u32 s29, s13, s2
	s_addc_u32 s31, s33, s3
	s_ashr_i32 s27, s26, 31
	s_lshl_b64 s[2:3], s[26:27], 19
	s_add_u32 s30, s29, s2
	s_addc_u32 s31, s31, s3
.LBB0_1755:
	s_nop 0
	v_cndmask_b32_e64 v0, 0, 1, s[4:5]
	v_cmp_ne_u32_e64 s[2:3], 1, v0
	s_andn2_b64 vcc, exec, s[4:5]
	s_mov_b64 s[34:35], s[44:45]
	s_mov_b64 s[36:37], s[42:43]
	s_cbranch_vccnz .LBB0_1757
	s_mov_b64 s[34:35], s[30:31]
	s_mov_b64 s[36:37], s[14:15]
	v_lshl_add_u32 v173, v248, 11, v164
	v_lshl_add_u32 v174, v249, 11, v165
	v_lshl_add_u32 v175, v250, 11, v164
	v_lshl_add_u32 v176, v251, 11, v165

.LBB0_3569:
	s_add_i32 s59, s59, 1
	s_mul_i32 s2, s59, s60
	s_mul_hi_u32 s3, s59, s56
	s_add_i32 s3, s3, s2
	s_mul_i32 s2, s59, s56
	s_add_u32 s2, s2, s8
	s_addc_u32 s3, s3, s9
	v_cmp_ge_i64_e32 vcc, s[2:3], v[150:151]
	v_cmp_lt_i64_e64 s[4:5], s[2:3], v[150:151]
	s_cbranch_vccnz .LBB0_3571
	s_ashr_i32 s3, s2, 31
	s_lshr_b32 s3, s3, 29
	s_add_i32 s3, s2, s3
	s_ashr_i32 s26, s3, 3
	s_and_b32 s3, s3, -8
	s_sub_i32 s2, s2, s3
	s_cmp_lt_i32 s2, 0
	s_cselect_b32 s3, s53, s10
	s_mul_i32 s2, s3, s2
	s_add_i32 s2, s2, s26
	s_ashr_i32 s3, s2, 31
	s_lshr_b32 s3, s3, 26
	s_add_i32 s3, s2, s3
	s_ashr_i32 s26, s3, 6
	s_lshl_b32 s27, s26, 3
	s_sub_i32 s26, s10, s27
	s_min_i32 s28, s26, 8
	s_abs_i32 s26, s28
	v_cvt_f32_u32_e32 v0, s26
	s_sub_i32 s30, 0, s26
	s_andn2_b32 s3, s3, 63
	s_sub_i32 s2, s2, s3
	v_rcp_iflag_f32_e32 v0, v0
	s_abs_i32 s3, s2
	s_xor_b32 s29, s2, s28
	s_ashr_i32 s29, s29, 31
	v_mul_f32_e32 v0, 0x4f7ffffe, v0
	v_cvt_u32_f32_e32 v0, v0
	s_nop 0
	v_readfirstlane_b32 s31, v0
	s_mul_i32 s30, s30, s31
	s_mul_hi_u32 s30, s31, s30
	s_add_i32 s31, s31, s30
	s_mul_hi_u32 s30, s3, s31
	s_mul_i32 s31, s30, s26
	s_sub_i32 s3, s3, s31
	s_add_i32 s34, s30, 1
	s_sub_i32 s31, s3, s26
	s_cmp_ge_u32 s3, s26
	s_cselect_b32 s30, s34, s30
	s_cselect_b32 s3, s31, s3
	s_add_i32 s31, s30, 1
	s_cmp_ge_u32 s3, s26
	s_cselect_b32 s3, s31, s30
	s_xor_b32 s3, s3, s29
	s_sub_i32 s26, s3, s29
	s_mul_i32 s3, s26, s28
	s_sub_i32 s2, s2, s3
	s_add_i32 s28, s2, s27
	s_ashr_i32 s29, s28, 31
	s_lshl_b64 s[2:3], s[28:29], 2
	s_add_u32 s2, s50, s2
	s_addc_u32 s3, s51, s3
	global_load_dword v177, v145, s[2:3]
	s_lshl_b32 s27, s28, 8
	v_add_u32_e32 v0, s27, v162
	v_add_u32_e32 v2, s27, v163
	s_bitset1_b32 s27, 7
	v_ashrrev_i32_e32 v1, 31, v0
	v_ashrrev_i32_e32 v3, 31, v2
	v_add_u32_e32 v4, s27, v162
	v_add_u32_e32 v6, s27, v163
	v_lshl_add_u64 v[0:1], v[0:1], 2, s[14:15]
	v_lshl_add_u64 v[2:3], v[2:3], 2, s[14:15]
	v_ashrrev_i32_e32 v5, 31, v4
	v_ashrrev_i32_e32 v7, 31, v6
	v_lshl_add_u64 v[4:5], v[4:5], 2, s[14:15]
	v_lshl_add_u64 v[6:7], v[6:7], 2, s[14:15]
	global_load_dword v248, v[0:1], off
	s_nop 0
	global_load_dword v249, v[2:3], off
	s_nop 0
	global_load_dword v250, v[4:5], off
	global_load_dword v251, v[6:7], off
	s_waitcnt vmcnt(0)
	v_readfirstlane_b32 s2, v177
	s_ashr_i32 s3, s2, 31
	s_lshl_b64 s[2:3], s[2:3], 22
	s_add_u32 s29, s11, s2
	s_addc_u32 s31, s33, s3
	s_ashr_i32 s27, s26, 31
	s_lshl_b64 s[2:3], s[26:27], 19
	s_add_u32 s30, s29, s2
	s_addc_u32 s31, s31, s3
.LBB0_3571:
	s_nop 0
	v_cndmask_b32_e64 v0, 0, 1, s[4:5]
	v_cmp_ne_u32_e64 s[2:3], 1, v0
	s_andn2_b64 vcc, exec, s[4:5]
	s_mov_b64 s[34:35], s[44:45]
	s_mov_b64 s[36:37], s[42:43]
	s_cbranch_vccnz .LBB0_3573
	s_mov_b64 s[34:35], s[30:31]
	s_mov_b64 s[36:37], s[12:13]
	v_lshl_add_u32 v173, v248, 11, v164
	v_lshl_add_u32 v174, v249, 11, v165
	v_lshl_add_u32 v175, v250, 11, v164
	v_lshl_add_u32 v176, v251, 11, v165
